# route pass 3: router bias loaded once per block instead of once per row (removes three fully waited loads that also drained the previous row's stores)
# speedup vs baseline: 1.0388x; 1.0011x over previous
.LBB0_1884:
	v_and_b32_e32 v62, 0xffffff00, v103
	v_lshl_add_u32 v63, v254, 2, v62
	v_lshlrev_b32_e32 v63, 2, v63
	global_load_dwordx4 v[200:203], v63, s[62:63]
	global_load_dwordx4 v[204:207], v63, s[34:35]
	global_load_dwordx4 v[208:211], v63, s[36:37]
	v_lshlrev_b32_e32 v64, 1, v103
	v_mov_b32_e32 v65, 0
	v_mov_b32_e32 v66, v103
	v_mov_b32_e32 v67, 0
	v_lshl_add_u64 v[196:197], v[48:49], 0, v[64:65]
	v_lshlrev_b32_e32 v68, 6, v62
	v_lshl_add_u32 v68, v254, 4, v68
	v_lshlrev_b32_e32 v69, 12, v75
	v_sub_u32_e32 v68, v68, v69
	v_ashrrev_i32_e32 v69, 31, v68
	v_lshl_add_u64 v[34:35], v[34:35], 0, v[68:69]
	v_lshl_add_u64 v[36:37], v[36:37], 0, v[68:69]
	v_lshl_add_u64 v[38:39], v[38:39], 0, v[68:69]
	v_lshl_add_u64 v[40:41], v[40:41], 0, v[68:69]
	v_mov_b32_e32 v198, 0x1000
	v_mov_b32_e32 v199, 0
	v_lshl_add_u64 v[72:73], v[50:51], 0, v[66:67]
	global_load_dwordx4 v[112:115], v[196:197], off
	global_load_dwordx4 v[116:119], v[34:35], off
	global_load_dwordx4 v[120:123], v[36:37], off
	global_load_dwordx4 v[124:127], v[38:39], off
	global_load_dwordx4 v[128:131], v[40:41], off
	global_load_dwordx4 v[132:135], v[196:197], off offset:32
	global_load_dwordx4 v[136:139], v[34:35], off offset:1024
	global_load_dwordx4 v[140:143], v[36:37], off offset:1024
	global_load_dwordx4 v[144:147], v[38:39], off offset:1024
	global_load_dwordx4 v[148:151], v[40:41], off offset:1024
	global_load_dwordx4 v[152:155], v[196:197], off offset:64
	global_load_dwordx4 v[156:159], v[34:35], off offset:2048
	global_load_dwordx4 v[160:163], v[36:37], off offset:2048
	global_load_dwordx4 v[164:167], v[38:39], off offset:2048
	global_load_dwordx4 v[168:171], v[40:41], off offset:2048
	global_load_dwordx4 v[172:175], v[196:197], off offset:96
	global_load_dwordx4 v[176:179], v[34:35], off offset:3072
	global_load_dwordx4 v[180:183], v[36:37], off offset:3072
	global_load_dwordx4 v[184:187], v[38:39], off offset:3072
	global_load_dwordx4 v[188:191], v[40:41], off offset:3072
	v_mul_u32_u24_e32 v62, 12, v62
	v_add_u32_e32 v62, 0x12000, v62
	v_lshl_add_u32 v1, v254, 4, v62
	v_and_b32_e32 v63, 8, v103
	v_lshl_add_u32 v111, v63, 2, v62
	s_waitcnt vmcnt(20)
	v_pk_add_f32 v[204:205], v[204:205], 1.0 op_sel_hi:[1,0]
	v_pk_add_f32 v[206:207], v[206:207], 1.0 op_sel_hi:[1,0]
	ds_write_b128 v1, v[200:203]
	ds_write_b128 v1, v[204:207] offset:1024
	ds_write_b128 v1, v[208:211] offset:2048
	s_waitcnt lgkmcnt(0)
	ds_read_b128 v[200:203], v111 offset:0
	ds_read_b128 v[204:207], v111 offset:16
	ds_read_b128 v[208:211], v111 offset:1024
	ds_read_b128 v[212:215], v111 offset:1040
	ds_read_b128 v[216:219], v111 offset:2048
	ds_read_b128 v[220:223], v111 offset:2064
	s_waitcnt lgkmcnt(0)
	ds_read_b128 v[224:227], v111 offset:64
	ds_read_b128 v[228:231], v111 offset:80
	ds_read_b128 v[232:235], v111 offset:1088
	ds_read_b128 v[236:239], v111 offset:1104
	ds_read_b128 v[240:243], v111 offset:2112
	ds_read_b128 v[244:247], v111 offset:2128
	s_waitcnt vmcnt(15)
	v_lshlrev_b32_e32 v54, 16, v112
	v_and_b32_e32 v55, 0xffff0000, v112
	v_lshlrev_b32_e32 v56, 16, v113
	v_and_b32_e32 v57, 0xffff0000, v113
	v_lshlrev_b32_e32 v58, 16, v114
	v_and_b32_e32 v59, 0xffff0000, v114
	v_lshlrev_b32_e32 v60, 16, v115
	v_and_b32_e32 v61, 0xffff0000, v115
	v_pk_mul_f32 v[54:55], v[46:47], v[54:55]
	v_pk_mul_f32 v[56:57], v[46:47], v[56:57]
	v_pk_mul_f32 v[58:59], v[46:47], v[58:59]
	v_pk_mul_f32 v[60:61], v[46:47], v[60:61]
	v_pk_mul_f32 v[54:55], v[200:201], v[54:55]
	v_pk_mul_f32 v[56:57], v[202:203], v[56:57]
	v_pk_mul_f32 v[58:59], v[204:205], v[58:59]
	v_pk_mul_f32 v[60:61], v[206:207], v[60:61]
	v_pk_fma_f32 v[54:55], v[208:209], v[54:55], v[216:217]
	v_pk_fma_f32 v[56:57], v[210:211], v[56:57], v[218:219]
	v_pk_fma_f32 v[58:59], v[212:213], v[58:59], v[220:221]
	v_pk_fma_f32 v[60:61], v[214:215], v[60:61], v[222:223]
	v_med3_f32 v62, v54, s82, v108
	v_med3_f32 v63, v55, s82, v108
	v_med3_f32 v64, v56, s82, v108
	v_med3_f32 v65, v57, s82, v108
	v_med3_f32 v66, v58, s82, v108
	v_med3_f32 v67, v59, s82, v108
	v_med3_f32 v68, v60, s82, v108
	v_med3_f32 v69, v61, s82, v108
	v_cvt_pk_bf16_f32 v192, v54, v55
	v_cvt_pk_bf16_f32 v193, v56, v57
	v_cvt_pk_bf16_f32 v194, v58, v59
	v_cvt_pk_bf16_f32 v195, v60, v61
	v_cvt_pk_fp8_f32 v70, v62, v63
	v_cvt_pk_fp8_f32 v71, v66, v67
	v_cvt_pk_fp8_f32 v70, v64, v65 op_sel:[0,0,1]
	v_cvt_pk_fp8_f32 v71, v68, v69 op_sel:[0,0,1]
	s_nop 0
	global_store_dwordx2 v[72:73], v[70:71], off
	v_mfma_f32_32x32x16_bf16 v[2:17], v[192:195], v[116:119], v[2:17]
	v_mfma_f32_32x32x16_bf16 v[18:33], v[192:195], v[120:123], v[18:33]
	v_mfma_f32_32x32x16_bf16 v[2:17], v[192:195], v[124:127], v[2:17]
	v_mfma_f32_32x32x16_bf16 v[18:33], v[192:195], v[128:131], v[18:33]
	v_lshlrev_b32_e32 v252, 16, v192
	v_and_b32_e32 v253, 0xffff0000, v192
	v_sub_f32_e32 v62, v54, v252
	v_sub_f32_e32 v63, v55, v253
	v_lshlrev_b32_e32 v252, 16, v193
	v_and_b32_e32 v253, 0xffff0000, v193
	v_sub_f32_e32 v64, v56, v252
	v_sub_f32_e32 v65, v57, v253
	v_lshlrev_b32_e32 v252, 16, v194
	v_and_b32_e32 v253, 0xffff0000, v194
	v_sub_f32_e32 v66, v58, v252
	v_sub_f32_e32 v67, v59, v253
	v_lshlrev_b32_e32 v252, 16, v195
	v_and_b32_e32 v253, 0xffff0000, v195
	v_sub_f32_e32 v68, v60, v252
	v_sub_f32_e32 v69, v61, v253
	v_cvt_pk_bf16_f32 v248, v62, v63
	v_cvt_pk_bf16_f32 v249, v64, v65
	v_cvt_pk_bf16_f32 v250, v66, v67
	v_cvt_pk_bf16_f32 v251, v68, v69
	s_nop 1
	v_mfma_f32_32x32x16_bf16 v[2:17], v[248:251], v[116:119], v[2:17]
	v_mfma_f32_32x32x16_bf16 v[18:33], v[248:251], v[120:123], v[18:33]
	global_load_dwordx4 v[112:115], v[196:197], off offset:128
	v_lshl_add_u64 v[34:35], v[34:35], 0, v[198:199]
	v_lshl_add_u64 v[36:37], v[36:37], 0, v[198:199]
	v_lshl_add_u64 v[38:39], v[38:39], 0, v[198:199]
	v_lshl_add_u64 v[40:41], v[40:41], 0, v[198:199]
	global_load_dwordx4 v[116:119], v[34:35], off
	global_load_dwordx4 v[120:123], v[36:37], off
	global_load_dwordx4 v[124:127], v[38:39], off
	global_load_dwordx4 v[128:131], v[40:41], off
	s_waitcnt lgkmcnt(0)
	ds_read_b128 v[200:203], v111 offset:128
	ds_read_b128 v[204:207], v111 offset:144
	ds_read_b128 v[208:211], v111 offset:1152
	ds_read_b128 v[212:215], v111 offset:1168
	ds_read_b128 v[216:219], v111 offset:2176
	ds_read_b128 v[220:223], v111 offset:2192
	s_waitcnt vmcnt(16)
	v_lshlrev_b32_e32 v54, 16, v132
	v_and_b32_e32 v55, 0xffff0000, v132
	v_lshlrev_b32_e32 v56, 16, v133
	v_and_b32_e32 v57, 0xffff0000, v133
	v_lshlrev_b32_e32 v58, 16, v134
	v_and_b32_e32 v59, 0xffff0000, v134
	v_lshlrev_b32_e32 v60, 16, v135
	v_and_b32_e32 v61, 0xffff0000, v135
	v_pk_mul_f32 v[54:55], v[46:47], v[54:55]
	v_pk_mul_f32 v[56:57], v[46:47], v[56:57]
	v_pk_mul_f32 v[58:59], v[46:47], v[58:59]
	v_pk_mul_f32 v[60:61], v[46:47], v[60:61]
	v_pk_mul_f32 v[54:55], v[224:225], v[54:55]
	v_pk_mul_f32 v[56:57], v[226:227], v[56:57]
	v_pk_mul_f32 v[58:59], v[228:229], v[58:59]
	v_pk_mul_f32 v[60:61], v[230:231], v[60:61]
	v_pk_fma_f32 v[54:55], v[232:233], v[54:55], v[240:241]
	v_pk_fma_f32 v[56:57], v[234:235], v[56:57], v[242:243]
	v_pk_fma_f32 v[58:59], v[236:237], v[58:59], v[244:245]
	v_pk_fma_f32 v[60:61], v[238:239], v[60:61], v[246:247]
	v_med3_f32 v62, v54, s82, v108
	v_med3_f32 v63, v55, s82, v108
	v_med3_f32 v64, v56, s82, v108
	v_med3_f32 v65, v57, s82, v108
	v_med3_f32 v66, v58, s82, v108
	v_med3_f32 v67, v59, s82, v108
	v_med3_f32 v68, v60, s82, v108
	v_med3_f32 v69, v61, s82, v108
	v_cvt_pk_bf16_f32 v192, v54, v55
	v_cvt_pk_bf16_f32 v193, v56, v57
	v_cvt_pk_bf16_f32 v194, v58, v59
	v_cvt_pk_bf16_f32 v195, v60, v61
	v_cvt_pk_fp8_f32 v70, v62, v63
	v_cvt_pk_fp8_f32 v71, v66, v67
	v_cvt_pk_fp8_f32 v70, v64, v65 op_sel:[0,0,1]
	v_cvt_pk_fp8_f32 v71, v68, v69 op_sel:[0,0,1]
	s_nop 0
	global_store_dwordx2 v[72:73], v[70:71], off offset:16
	v_mfma_f32_32x32x16_bf16 v[2:17], v[192:195], v[136:139], v[2:17]
	v_mfma_f32_32x32x16_bf16 v[18:33], v[192:195], v[140:143], v[18:33]
	v_mfma_f32_32x32x16_bf16 v[2:17], v[192:195], v[144:147], v[2:17]
	v_mfma_f32_32x32x16_bf16 v[18:33], v[192:195], v[148:151], v[18:33]
	v_lshlrev_b32_e32 v252, 16, v192
	v_and_b32_e32 v253, 0xffff0000, v192
	v_sub_f32_e32 v62, v54, v252
	v_sub_f32_e32 v63, v55, v253
	v_lshlrev_b32_e32 v252, 16, v193
	v_and_b32_e32 v253, 0xffff0000, v193
	v_sub_f32_e32 v64, v56, v252
	v_sub_f32_e32 v65, v57, v253
	v_lshlrev_b32_e32 v252, 16, v194
	v_and_b32_e32 v253, 0xffff0000, v194
	v_sub_f32_e32 v66, v58, v252
	v_sub_f32_e32 v67, v59, v253
	v_lshlrev_b32_e32 v252, 16, v195
	v_and_b32_e32 v253, 0xffff0000, v195
	v_sub_f32_e32 v68, v60, v252
	v_sub_f32_e32 v69, v61, v253
	v_cvt_pk_bf16_f32 v248, v62, v63
	v_cvt_pk_bf16_f32 v249, v64, v65
	v_cvt_pk_bf16_f32 v250, v66, v67
	v_cvt_pk_bf16_f32 v251, v68, v69
	s_nop 1
	v_mfma_f32_32x32x16_bf16 v[2:17], v[248:251], v[136:139], v[2:17]
	v_mfma_f32_32x32x16_bf16 v[18:33], v[248:251], v[140:143], v[18:33]
	global_load_dwordx4 v[132:135], v[196:197], off offset:160
	global_load_dwordx4 v[136:139], v[34:35], off offset:1024
	global_load_dwordx4 v[140:143], v[36:37], off offset:1024
	global_load_dwordx4 v[144:147], v[38:39], off offset:1024
	global_load_dwordx4 v[148:151], v[40:41], off offset:1024
	s_waitcnt lgkmcnt(0)
	ds_read_b128 v[224:227], v111 offset:192
	ds_read_b128 v[228:231], v111 offset:208
	ds_read_b128 v[232:235], v111 offset:1216
	ds_read_b128 v[236:239], v111 offset:1232
	ds_read_b128 v[240:243], v111 offset:2240
	ds_read_b128 v[244:247], v111 offset:2256
	s_waitcnt vmcnt(17)
	v_lshlrev_b32_e32 v54, 16, v152
	v_and_b32_e32 v55, 0xffff0000, v152
	v_lshlrev_b32_e32 v56, 16, v153
	v_and_b32_e32 v57, 0xffff0000, v153
	v_lshlrev_b32_e32 v58, 16, v154
	v_and_b32_e32 v59, 0xffff0000, v154
	v_lshlrev_b32_e32 v60, 16, v155
	v_and_b32_e32 v61, 0xffff0000, v155
	v_pk_mul_f32 v[54:55], v[46:47], v[54:55]
	v_pk_mul_f32 v[56:57], v[46:47], v[56:57]
	v_pk_mul_f32 v[58:59], v[46:47], v[58:59]
	v_pk_mul_f32 v[60:61], v[46:47], v[60:61]
	v_pk_mul_f32 v[54:55], v[200:201], v[54:55]
	v_pk_mul_f32 v[56:57], v[202:203], v[56:57]
	v_pk_mul_f32 v[58:59], v[204:205], v[58:59]
	v_pk_mul_f32 v[60:61], v[206:207], v[60:61]
	v_pk_fma_f32 v[54:55], v[208:209], v[54:55], v[216:217]
	v_pk_fma_f32 v[56:57], v[210:211], v[56:57], v[218:219]
	v_pk_fma_f32 v[58:59], v[212:213], v[58:59], v[220:221]
	v_pk_fma_f32 v[60:61], v[214:215], v[60:61], v[222:223]
	v_med3_f32 v62, v54, s82, v108
	v_med3_f32 v63, v55, s82, v108
	v_med3_f32 v64, v56, s82, v108
	v_med3_f32 v65, v57, s82, v108
	v_med3_f32 v66, v58, s82, v108
	v_med3_f32 v67, v59, s82, v108
	v_med3_f32 v68, v60, s82, v108
	v_med3_f32 v69, v61, s82, v108
	v_cvt_pk_bf16_f32 v192, v54, v55
	v_cvt_pk_bf16_f32 v193, v56, v57
	v_cvt_pk_bf16_f32 v194, v58, v59
	v_cvt_pk_bf16_f32 v195, v60, v61
	v_cvt_pk_fp8_f32 v70, v62, v63
	v_cvt_pk_fp8_f32 v71, v66, v67
	v_cvt_pk_fp8_f32 v70, v64, v65 op_sel:[0,0,1]
	v_cvt_pk_fp8_f32 v71, v68, v69 op_sel:[0,0,1]
	s_nop 0
	global_store_dwordx2 v[72:73], v[70:71], off offset:32
	v_mfma_f32_32x32x16_bf16 v[2:17], v[192:195], v[156:159], v[2:17]
	v_mfma_f32_32x32x16_bf16 v[18:33], v[192:195], v[160:163], v[18:33]
	v_mfma_f32_32x32x16_bf16 v[2:17], v[192:195], v[164:167], v[2:17]
	v_mfma_f32_32x32x16_bf16 v[18:33], v[192:195], v[168:171], v[18:33]
	v_lshlrev_b32_e32 v252, 16, v192
	v_and_b32_e32 v253, 0xffff0000, v192
	v_sub_f32_e32 v62, v54, v252
	v_sub_f32_e32 v63, v55, v253
	v_lshlrev_b32_e32 v252, 16, v193
	v_and_b32_e32 v253, 0xffff0000, v193
	v_sub_f32_e32 v64, v56, v252
	v_sub_f32_e32 v65, v57, v253
	v_lshlrev_b32_e32 v252, 16, v194
	v_and_b32_e32 v253, 0xffff0000, v194
	v_sub_f32_e32 v66, v58, v252
	v_sub_f32_e32 v67, v59, v253
	v_lshlrev_b32_e32 v252, 16, v195
	v_and_b32_e32 v253, 0xffff0000, v195
	v_sub_f32_e32 v68, v60, v252
	v_sub_f32_e32 v69, v61, v253
	v_cvt_pk_bf16_f32 v248, v62, v63
	v_cvt_pk_bf16_f32 v249, v64, v65
	v_cvt_pk_bf16_f32 v250, v66, v67
	v_cvt_pk_bf16_f32 v251, v68, v69
	s_nop 1
	v_mfma_f32_32x32x16_bf16 v[2:17], v[248:251], v[156:159], v[2:17]
	v_mfma_f32_32x32x16_bf16 v[18:33], v[248:251], v[160:163], v[18:33]
	global_load_dwordx4 v[152:155], v[196:197], off offset:192
	global_load_dwordx4 v[156:159], v[34:35], off offset:2048
	global_load_dwordx4 v[160:163], v[36:37], off offset:2048
	global_load_dwordx4 v[164:167], v[38:39], off offset:2048
	global_load_dwordx4 v[168:171], v[40:41], off offset:2048
	s_waitcnt lgkmcnt(0)
	ds_read_b128 v[200:203], v111 offset:256
	ds_read_b128 v[204:207], v111 offset:272
	ds_read_b128 v[208:211], v111 offset:1280
	ds_read_b128 v[212:215], v111 offset:1296
	ds_read_b128 v[216:219], v111 offset:2304
	ds_read_b128 v[220:223], v111 offset:2320
	s_waitcnt vmcnt(18)
	v_lshlrev_b32_e32 v54, 16, v172
	v_and_b32_e32 v55, 0xffff0000, v172
	v_lshlrev_b32_e32 v56, 16, v173
	v_and_b32_e32 v57, 0xffff0000, v173
	v_lshlrev_b32_e32 v58, 16, v174
	v_and_b32_e32 v59, 0xffff0000, v174
	v_lshlrev_b32_e32 v60, 16, v175
	v_and_b32_e32 v61, 0xffff0000, v175
	v_pk_mul_f32 v[54:55], v[46:47], v[54:55]
	v_pk_mul_f32 v[56:57], v[46:47], v[56:57]
	v_pk_mul_f32 v[58:59], v[46:47], v[58:59]
	v_pk_mul_f32 v[60:61], v[46:47], v[60:61]
	v_pk_mul_f32 v[54:55], v[224:225], v[54:55]
	v_pk_mul_f32 v[56:57], v[226:227], v[56:57]
	v_pk_mul_f32 v[58:59], v[228:229], v[58:59]
	v_pk_mul_f32 v[60:61], v[230:231], v[60:61]
	v_pk_fma_f32 v[54:55], v[232:233], v[54:55], v[240:241]
	v_pk_fma_f32 v[56:57], v[234:235], v[56:57], v[242:243]
	v_pk_fma_f32 v[58:59], v[236:237], v[58:59], v[244:245]
	v_pk_fma_f32 v[60:61], v[238:239], v[60:61], v[246:247]
	v_med3_f32 v62, v54, s82, v108
	v_med3_f32 v63, v55, s82, v108
	v_med3_f32 v64, v56, s82, v108
	v_med3_f32 v65, v57, s82, v108
	v_med3_f32 v66, v58, s82, v108
	v_med3_f32 v67, v59, s82, v108
	v_med3_f32 v68, v60, s82, v108
	v_med3_f32 v69, v61, s82, v108
	v_cvt_pk_bf16_f32 v192, v54, v55
	v_cvt_pk_bf16_f32 v193, v56, v57
	v_cvt_pk_bf16_f32 v194, v58, v59
	v_cvt_pk_bf16_f32 v195, v60, v61
	v_cvt_pk_fp8_f32 v70, v62, v63
	v_cvt_pk_fp8_f32 v71, v66, v67
	v_cvt_pk_fp8_f32 v70, v64, v65 op_sel:[0,0,1]
	v_cvt_pk_fp8_f32 v71, v68, v69 op_sel:[0,0,1]
	s_nop 0
	global_store_dwordx2 v[72:73], v[70:71], off offset:48
	v_mfma_f32_32x32x16_bf16 v[2:17], v[192:195], v[176:179], v[2:17]
	v_mfma_f32_32x32x16_bf16 v[18:33], v[192:195], v[180:183], v[18:33]
	v_mfma_f32_32x32x16_bf16 v[2:17], v[192:195], v[184:187], v[2:17]
	v_mfma_f32_32x32x16_bf16 v[18:33], v[192:195], v[188:191], v[18:33]
	v_lshlrev_b32_e32 v252, 16, v192
	v_and_b32_e32 v253, 0xffff0000, v192
	v_sub_f32_e32 v62, v54, v252
	v_sub_f32_e32 v63, v55, v253
	v_lshlrev_b32_e32 v252, 16, v193
	v_and_b32_e32 v253, 0xffff0000, v193
	v_sub_f32_e32 v64, v56, v252
	v_sub_f32_e32 v65, v57, v253
	v_lshlrev_b32_e32 v252, 16, v194
	v_and_b32_e32 v253, 0xffff0000, v194
	v_sub_f32_e32 v66, v58, v252
	v_sub_f32_e32 v67, v59, v253
	v_lshlrev_b32_e32 v252, 16, v195
	v_and_b32_e32 v253, 0xffff0000, v195
	v_sub_f32_e32 v68, v60, v252
	v_sub_f32_e32 v69, v61, v253
	v_cvt_pk_bf16_f32 v248, v62, v63
	v_cvt_pk_bf16_f32 v249, v64, v65
	v_cvt_pk_bf16_f32 v250, v66, v67
	v_cvt_pk_bf16_f32 v251, v68, v69
	s_nop 1
	v_mfma_f32_32x32x16_bf16 v[2:17], v[248:251], v[176:179], v[2:17]
	v_mfma_f32_32x32x16_bf16 v[18:33], v[248:251], v[180:183], v[18:33]
	global_load_dwordx4 v[172:175], v[196:197], off offset:224
	global_load_dwordx4 v[176:179], v[34:35], off offset:3072
	global_load_dwordx4 v[180:183], v[36:37], off offset:3072
	global_load_dwordx4 v[184:187], v[38:39], off offset:3072
	global_load_dwordx4 v[188:191], v[40:41], off offset:3072
	s_waitcnt lgkmcnt(0)
	ds_read_b128 v[224:227], v111 offset:320
	ds_read_b128 v[228:231], v111 offset:336
	ds_read_b128 v[232:235], v111 offset:1344
	ds_read_b128 v[236:239], v111 offset:1360
	ds_read_b128 v[240:243], v111 offset:2368
	ds_read_b128 v[244:247], v111 offset:2384
	s_waitcnt vmcnt(18)
	v_lshlrev_b32_e32 v54, 16, v112
	v_and_b32_e32 v55, 0xffff0000, v112
	v_lshlrev_b32_e32 v56, 16, v113
	v_and_b32_e32 v57, 0xffff0000, v113
	v_lshlrev_b32_e32 v58, 16, v114
	v_and_b32_e32 v59, 0xffff0000, v114
	v_lshlrev_b32_e32 v60, 16, v115
	v_and_b32_e32 v61, 0xffff0000, v115
	v_pk_mul_f32 v[54:55], v[46:47], v[54:55]
	v_pk_mul_f32 v[56:57], v[46:47], v[56:57]
	v_pk_mul_f32 v[58:59], v[46:47], v[58:59]
	v_pk_mul_f32 v[60:61], v[46:47], v[60:61]
	v_pk_mul_f32 v[54:55], v[200:201], v[54:55]
	v_pk_mul_f32 v[56:57], v[202:203], v[56:57]
	v_pk_mul_f32 v[58:59], v[204:205], v[58:59]
	v_pk_mul_f32 v[60:61], v[206:207], v[60:61]
	v_pk_fma_f32 v[54:55], v[208:209], v[54:55], v[216:217]
	v_pk_fma_f32 v[56:57], v[210:211], v[56:57], v[218:219]
	v_pk_fma_f32 v[58:59], v[212:213], v[58:59], v[220:221]
	v_pk_fma_f32 v[60:61], v[214:215], v[60:61], v[222:223]
	v_med3_f32 v62, v54, s82, v108
	v_med3_f32 v63, v55, s82, v108
	v_med3_f32 v64, v56, s82, v108
	v_med3_f32 v65, v57, s82, v108
	v_med3_f32 v66, v58, s82, v108
	v_med3_f32 v67, v59, s82, v108
	v_med3_f32 v68, v60, s82, v108
	v_med3_f32 v69, v61, s82, v108
	v_cvt_pk_bf16_f32 v192, v54, v55
	v_cvt_pk_bf16_f32 v193, v56, v57
	v_cvt_pk_bf16_f32 v194, v58, v59
	v_cvt_pk_bf16_f32 v195, v60, v61
	v_cvt_pk_fp8_f32 v70, v62, v63
	v_cvt_pk_fp8_f32 v71, v66, v67
	v_cvt_pk_fp8_f32 v70, v64, v65 op_sel:[0,0,1]
	v_cvt_pk_fp8_f32 v71, v68, v69 op_sel:[0,0,1]
	s_nop 0
	global_store_dwordx2 v[72:73], v[70:71], off offset:64
	v_mfma_f32_32x32x16_bf16 v[2:17], v[192:195], v[116:119], v[2:17]
	v_mfma_f32_32x32x16_bf16 v[18:33], v[192:195], v[120:123], v[18:33]
	v_mfma_f32_32x32x16_bf16 v[2:17], v[192:195], v[124:127], v[2:17]
	v_mfma_f32_32x32x16_bf16 v[18:33], v[192:195], v[128:131], v[18:33]
	v_lshlrev_b32_e32 v252, 16, v192
	v_and_b32_e32 v253, 0xffff0000, v192
	v_sub_f32_e32 v62, v54, v252
	v_sub_f32_e32 v63, v55, v253
	v_lshlrev_b32_e32 v252, 16, v193
	v_and_b32_e32 v253, 0xffff0000, v193
	v_sub_f32_e32 v64, v56, v252
	v_sub_f32_e32 v65, v57, v253
	v_lshlrev_b32_e32 v252, 16, v194
	v_and_b32_e32 v253, 0xffff0000, v194
	v_sub_f32_e32 v66, v58, v252
	v_sub_f32_e32 v67, v59, v253
	v_lshlrev_b32_e32 v252, 16, v195
	v_and_b32_e32 v253, 0xffff0000, v195
	v_sub_f32_e32 v68, v60, v252
	v_sub_f32_e32 v69, v61, v253
	v_cvt_pk_bf16_f32 v248, v62, v63
	v_cvt_pk_bf16_f32 v249, v64, v65
	v_cvt_pk_bf16_f32 v250, v66, v67
	v_cvt_pk_bf16_f32 v251, v68, v69
	s_nop 1
	v_mfma_f32_32x32x16_bf16 v[2:17], v[248:251], v[116:119], v[2:17]
	v_mfma_f32_32x32x16_bf16 v[18:33], v[248:251], v[120:123], v[18:33]
	global_load_dwordx4 v[112:115], v[196:197], off offset:256
	v_lshl_add_u64 v[34:35], v[34:35], 0, v[198:199]
	v_lshl_add_u64 v[36:37], v[36:37], 0, v[198:199]
	v_lshl_add_u64 v[38:39], v[38:39], 0, v[198:199]
	v_lshl_add_u64 v[40:41], v[40:41], 0, v[198:199]
	global_load_dwordx4 v[116:119], v[34:35], off
	global_load_dwordx4 v[120:123], v[36:37], off
	global_load_dwordx4 v[124:127], v[38:39], off
	global_load_dwordx4 v[128:131], v[40:41], off
	s_waitcnt lgkmcnt(0)
	ds_read_b128 v[200:203], v111 offset:384
	ds_read_b128 v[204:207], v111 offset:400
	ds_read_b128 v[208:211], v111 offset:1408
	ds_read_b128 v[212:215], v111 offset:1424
	ds_read_b128 v[216:219], v111 offset:2432
	ds_read_b128 v[220:223], v111 offset:2448
	s_waitcnt vmcnt(18)
	v_lshlrev_b32_e32 v54, 16, v132
	v_and_b32_e32 v55, 0xffff0000, v132
	v_lshlrev_b32_e32 v56, 16, v133
	v_and_b32_e32 v57, 0xffff0000, v133
	v_lshlrev_b32_e32 v58, 16, v134
	v_and_b32_e32 v59, 0xffff0000, v134
	v_lshlrev_b32_e32 v60, 16, v135
	v_and_b32_e32 v61, 0xffff0000, v135
	v_pk_mul_f32 v[54:55], v[46:47], v[54:55]
	v_pk_mul_f32 v[56:57], v[46:47], v[56:57]
	v_pk_mul_f32 v[58:59], v[46:47], v[58:59]
	v_pk_mul_f32 v[60:61], v[46:47], v[60:61]
	v_pk_mul_f32 v[54:55], v[224:225], v[54:55]
	v_pk_mul_f32 v[56:57], v[226:227], v[56:57]
	v_pk_mul_f32 v[58:59], v[228:229], v[58:59]
	v_pk_mul_f32 v[60:61], v[230:231], v[60:61]
	v_pk_fma_f32 v[54:55], v[232:233], v[54:55], v[240:241]
	v_pk_fma_f32 v[56:57], v[234:235], v[56:57], v[242:243]
	v_pk_fma_f32 v[58:59], v[236:237], v[58:59], v[244:245]
	v_pk_fma_f32 v[60:61], v[238:239], v[60:61], v[246:247]
	v_med3_f32 v62, v54, s82, v108
	v_med3_f32 v63, v55, s82, v108
	v_med3_f32 v64, v56, s82, v108
	v_med3_f32 v65, v57, s82, v108
	v_med3_f32 v66, v58, s82, v108
	v_med3_f32 v67, v59, s82, v108
	v_med3_f32 v68, v60, s82, v108
	v_med3_f32 v69, v61, s82, v108
	v_cvt_pk_bf16_f32 v192, v54, v55
	v_cvt_pk_bf16_f32 v193, v56, v57
	v_cvt_pk_bf16_f32 v194, v58, v59
	v_cvt_pk_bf16_f32 v195, v60, v61
	v_cvt_pk_fp8_f32 v70, v62, v63
	v_cvt_pk_fp8_f32 v71, v66, v67
	v_cvt_pk_fp8_f32 v70, v64, v65 op_sel:[0,0,1]
	v_cvt_pk_fp8_f32 v71, v68, v69 op_sel:[0,0,1]
	s_nop 0
	global_store_dwordx2 v[72:73], v[70:71], off offset:80
	v_mfma_f32_32x32x16_bf16 v[2:17], v[192:195], v[136:139], v[2:17]
	v_mfma_f32_32x32x16_bf16 v[18:33], v[192:195], v[140:143], v[18:33]
	v_mfma_f32_32x32x16_bf16 v[2:17], v[192:195], v[144:147], v[2:17]
	v_mfma_f32_32x32x16_bf16 v[18:33], v[192:195], v[148:151], v[18:33]
	v_lshlrev_b32_e32 v252, 16, v192
	v_and_b32_e32 v253, 0xffff0000, v192
	v_sub_f32_e32 v62, v54, v252
	v_sub_f32_e32 v63, v55, v253
	v_lshlrev_b32_e32 v252, 16, v193
	v_and_b32_e32 v253, 0xffff0000, v193
	v_sub_f32_e32 v64, v56, v252
	v_sub_f32_e32 v65, v57, v253
	v_lshlrev_b32_e32 v252, 16, v194
	v_and_b32_e32 v253, 0xffff0000, v194
	v_sub_f32_e32 v66, v58, v252
	v_sub_f32_e32 v67, v59, v253
	v_lshlrev_b32_e32 v252, 16, v195
	v_and_b32_e32 v253, 0xffff0000, v195
	v_sub_f32_e32 v68, v60, v252
	v_sub_f32_e32 v69, v61, v253
	v_cvt_pk_bf16_f32 v248, v62, v63
	v_cvt_pk_bf16_f32 v249, v64, v65
	v_cvt_pk_bf16_f32 v250, v66, v67
	v_cvt_pk_bf16_f32 v251, v68, v69
	s_nop 1
	v_mfma_f32_32x32x16_bf16 v[2:17], v[248:251], v[136:139], v[2:17]
	v_mfma_f32_32x32x16_bf16 v[18:33], v[248:251], v[140:143], v[18:33]
	global_load_dwordx4 v[132:135], v[196:197], off offset:288
	global_load_dwordx4 v[136:139], v[34:35], off offset:1024
	global_load_dwordx4 v[140:143], v[36:37], off offset:1024
	global_load_dwordx4 v[144:147], v[38:39], off offset:1024
	global_load_dwordx4 v[148:151], v[40:41], off offset:1024
	s_waitcnt lgkmcnt(0)
	ds_read_b128 v[224:227], v111 offset:448
	ds_read_b128 v[228:231], v111 offset:464
	ds_read_b128 v[232:235], v111 offset:1472
	ds_read_b128 v[236:239], v111 offset:1488
	ds_read_b128 v[240:243], v111 offset:2496
	ds_read_b128 v[244:247], v111 offset:2512
	s_waitcnt vmcnt(18)
	v_lshlrev_b32_e32 v54, 16, v152
	v_and_b32_e32 v55, 0xffff0000, v152
	v_lshlrev_b32_e32 v56, 16, v153
	v_and_b32_e32 v57, 0xffff0000, v153
	v_lshlrev_b32_e32 v58, 16, v154
	v_and_b32_e32 v59, 0xffff0000, v154
	v_lshlrev_b32_e32 v60, 16, v155
	v_and_b32_e32 v61, 0xffff0000, v155
	v_pk_mul_f32 v[54:55], v[46:47], v[54:55]
	v_pk_mul_f32 v[56:57], v[46:47], v[56:57]
	v_pk_mul_f32 v[58:59], v[46:47], v[58:59]
	v_pk_mul_f32 v[60:61], v[46:47], v[60:61]
	v_pk_mul_f32 v[54:55], v[200:201], v[54:55]
	v_pk_mul_f32 v[56:57], v[202:203], v[56:57]
	v_pk_mul_f32 v[58:59], v[204:205], v[58:59]
	v_pk_mul_f32 v[60:61], v[206:207], v[60:61]
	v_pk_fma_f32 v[54:55], v[208:209], v[54:55], v[216:217]
	v_pk_fma_f32 v[56:57], v[210:211], v[56:57], v[218:219]
	v_pk_fma_f32 v[58:59], v[212:213], v[58:59], v[220:221]
	v_pk_fma_f32 v[60:61], v[214:215], v[60:61], v[222:223]
	v_med3_f32 v62, v54, s82, v108
	v_med3_f32 v63, v55, s82, v108
	v_med3_f32 v64, v56, s82, v108
	v_med3_f32 v65, v57, s82, v108
	v_med3_f32 v66, v58, s82, v108
	v_med3_f32 v67, v59, s82, v108
	v_med3_f32 v68, v60, s82, v108
	v_med3_f32 v69, v61, s82, v108
	v_cvt_pk_bf16_f32 v192, v54, v55
	v_cvt_pk_bf16_f32 v193, v56, v57
	v_cvt_pk_bf16_f32 v194, v58, v59
	v_cvt_pk_bf16_f32 v195, v60, v61
	v_cvt_pk_fp8_f32 v70, v62, v63
	v_cvt_pk_fp8_f32 v71, v66, v67
	v_cvt_pk_fp8_f32 v70, v64, v65 op_sel:[0,0,1]
	v_cvt_pk_fp8_f32 v71, v68, v69 op_sel:[0,0,1]
	s_nop 0
	global_store_dwordx2 v[72:73], v[70:71], off offset:96
	v_mfma_f32_32x32x16_bf16 v[2:17], v[192:195], v[156:159], v[2:17]
	v_mfma_f32_32x32x16_bf16 v[18:33], v[192:195], v[160:163], v[18:33]
	v_mfma_f32_32x32x16_bf16 v[2:17], v[192:195], v[164:167], v[2:17]
	v_mfma_f32_32x32x16_bf16 v[18:33], v[192:195], v[168:171], v[18:33]
	v_lshlrev_b32_e32 v252, 16, v192
	v_and_b32_e32 v253, 0xffff0000, v192
	v_sub_f32_e32 v62, v54, v252
	v_sub_f32_e32 v63, v55, v253
	v_lshlrev_b32_e32 v252, 16, v193
	v_and_b32_e32 v253, 0xffff0000, v193
	v_sub_f32_e32 v64, v56, v252
	v_sub_f32_e32 v65, v57, v253
	v_lshlrev_b32_e32 v252, 16, v194
	v_and_b32_e32 v253, 0xffff0000, v194
	v_sub_f32_e32 v66, v58, v252
	v_sub_f32_e32 v67, v59, v253
	v_lshlrev_b32_e32 v252, 16, v195
	v_and_b32_e32 v253, 0xffff0000, v195
	v_sub_f32_e32 v68, v60, v252
	v_sub_f32_e32 v69, v61, v253
	v_cvt_pk_bf16_f32 v248, v62, v63
	v_cvt_pk_bf16_f32 v249, v64, v65
	v_cvt_pk_bf16_f32 v250, v66, v67
	v_cvt_pk_bf16_f32 v251, v68, v69
	s_nop 1
	v_mfma_f32_32x32x16_bf16 v[2:17], v[248:251], v[156:159], v[2:17]
	v_mfma_f32_32x32x16_bf16 v[18:33], v[248:251], v[160:163], v[18:33]
	global_load_dwordx4 v[152:155], v[196:197], off offset:320
	global_load_dwordx4 v[156:159], v[34:35], off offset:2048
	global_load_dwordx4 v[160:163], v[36:37], off offset:2048
	global_load_dwordx4 v[164:167], v[38:39], off offset:2048
	global_load_dwordx4 v[168:171], v[40:41], off offset:2048
	s_waitcnt lgkmcnt(0)
	ds_read_b128 v[200:203], v111 offset:512
	ds_read_b128 v[204:207], v111 offset:528
	ds_read_b128 v[208:211], v111 offset:1536
	ds_read_b128 v[212:215], v111 offset:1552
	ds_read_b128 v[216:219], v111 offset:2560
	ds_read_b128 v[220:223], v111 offset:2576
	s_waitcnt vmcnt(18)
	v_lshlrev_b32_e32 v54, 16, v172
	v_and_b32_e32 v55, 0xffff0000, v172
	v_lshlrev_b32_e32 v56, 16, v173
	v_and_b32_e32 v57, 0xffff0000, v173
	v_lshlrev_b32_e32 v58, 16, v174
	v_and_b32_e32 v59, 0xffff0000, v174
	v_lshlrev_b32_e32 v60, 16, v175
	v_and_b32_e32 v61, 0xffff0000, v175
	v_pk_mul_f32 v[54:55], v[46:47], v[54:55]
	v_pk_mul_f32 v[56:57], v[46:47], v[56:57]
	v_pk_mul_f32 v[58:59], v[46:47], v[58:59]
	v_pk_mul_f32 v[60:61], v[46:47], v[60:61]
	v_pk_mul_f32 v[54:55], v[224:225], v[54:55]
	v_pk_mul_f32 v[56:57], v[226:227], v[56:57]
	v_pk_mul_f32 v[58:59], v[228:229], v[58:59]
	v_pk_mul_f32 v[60:61], v[230:231], v[60:61]
	v_pk_fma_f32 v[54:55], v[232:233], v[54:55], v[240:241]
	v_pk_fma_f32 v[56:57], v[234:235], v[56:57], v[242:243]
	v_pk_fma_f32 v[58:59], v[236:237], v[58:59], v[244:245]
	v_pk_fma_f32 v[60:61], v[238:239], v[60:61], v[246:247]
	v_med3_f32 v62, v54, s82, v108
	v_med3_f32 v63, v55, s82, v108
	v_med3_f32 v64, v56, s82, v108
	v_med3_f32 v65, v57, s82, v108
	v_med3_f32 v66, v58, s82, v108
	v_med3_f32 v67, v59, s82, v108
	v_med3_f32 v68, v60, s82, v108
	v_med3_f32 v69, v61, s82, v108
	v_cvt_pk_bf16_f32 v192, v54, v55
	v_cvt_pk_bf16_f32 v193, v56, v57
	v_cvt_pk_bf16_f32 v194, v58, v59
	v_cvt_pk_bf16_f32 v195, v60, v61
	v_cvt_pk_fp8_f32 v70, v62, v63
	v_cvt_pk_fp8_f32 v71, v66, v67
	v_cvt_pk_fp8_f32 v70, v64, v65 op_sel:[0,0,1]
	v_cvt_pk_fp8_f32 v71, v68, v69 op_sel:[0,0,1]
	s_nop 0
	global_store_dwordx2 v[72:73], v[70:71], off offset:112
	v_mfma_f32_32x32x16_bf16 v[2:17], v[192:195], v[176:179], v[2:17]
	v_mfma_f32_32x32x16_bf16 v[18:33], v[192:195], v[180:183], v[18:33]
	v_mfma_f32_32x32x16_bf16 v[2:17], v[192:195], v[184:187], v[2:17]
	v_mfma_f32_32x32x16_bf16 v[18:33], v[192:195], v[188:191], v[18:33]
	v_lshlrev_b32_e32 v252, 16, v192
	v_and_b32_e32 v253, 0xffff0000, v192
	v_sub_f32_e32 v62, v54, v252
	v_sub_f32_e32 v63, v55, v253
	v_lshlrev_b32_e32 v252, 16, v193
	v_and_b32_e32 v253, 0xffff0000, v193
	v_sub_f32_e32 v64, v56, v252
	v_sub_f32_e32 v65, v57, v253
	v_lshlrev_b32_e32 v252, 16, v194
	v_and_b32_e32 v253, 0xffff0000, v194
	v_sub_f32_e32 v66, v58, v252
	v_sub_f32_e32 v67, v59, v253
	v_lshlrev_b32_e32 v252, 16, v195
	v_and_b32_e32 v253, 0xffff0000, v195
	v_sub_f32_e32 v68, v60, v252
	v_sub_f32_e32 v69, v61, v253
	v_cvt_pk_bf16_f32 v248, v62, v63
	v_cvt_pk_bf16_f32 v249, v64, v65
	v_cvt_pk_bf16_f32 v250, v66, v67
	v_cvt_pk_bf16_f32 v251, v68, v69
	s_nop 1
	v_mfma_f32_32x32x16_bf16 v[2:17], v[248:251], v[176:179], v[2:17]
	v_mfma_f32_32x32x16_bf16 v[18:33], v[248:251], v[180:183], v[18:33]
	global_load_dwordx4 v[172:175], v[196:197], off offset:352
	global_load_dwordx4 v[176:179], v[34:35], off offset:3072
	global_load_dwordx4 v[180:183], v[36:37], off offset:3072
	global_load_dwordx4 v[184:187], v[38:39], off offset:3072
	global_load_dwordx4 v[188:191], v[40:41], off offset:3072
	s_waitcnt lgkmcnt(0)
	ds_read_b128 v[224:227], v111 offset:576
	ds_read_b128 v[228:231], v111 offset:592
	ds_read_b128 v[232:235], v111 offset:1600
	ds_read_b128 v[236:239], v111 offset:1616
	ds_read_b128 v[240:243], v111 offset:2624
	ds_read_b128 v[244:247], v111 offset:2640
	s_waitcnt vmcnt(18)
	v_lshlrev_b32_e32 v54, 16, v112
	v_and_b32_e32 v55, 0xffff0000, v112
	v_lshlrev_b32_e32 v56, 16, v113
	v_and_b32_e32 v57, 0xffff0000, v113
	v_lshlrev_b32_e32 v58, 16, v114
	v_and_b32_e32 v59, 0xffff0000, v114
	v_lshlrev_b32_e32 v60, 16, v115
	v_and_b32_e32 v61, 0xffff0000, v115
	v_pk_mul_f32 v[54:55], v[46:47], v[54:55]
	v_pk_mul_f32 v[56:57], v[46:47], v[56:57]
	v_pk_mul_f32 v[58:59], v[46:47], v[58:59]
	v_pk_mul_f32 v[60:61], v[46:47], v[60:61]
	v_pk_mul_f32 v[54:55], v[200:201], v[54:55]
	v_pk_mul_f32 v[56:57], v[202:203], v[56:57]
	v_pk_mul_f32 v[58:59], v[204:205], v[58:59]
	v_pk_mul_f32 v[60:61], v[206:207], v[60:61]
	v_pk_fma_f32 v[54:55], v[208:209], v[54:55], v[216:217]
	v_pk_fma_f32 v[56:57], v[210:211], v[56:57], v[218:219]
	v_pk_fma_f32 v[58:59], v[212:213], v[58:59], v[220:221]
	v_pk_fma_f32 v[60:61], v[214:215], v[60:61], v[222:223]
	v_med3_f32 v62, v54, s82, v108
	v_med3_f32 v63, v55, s82, v108
	v_med3_f32 v64, v56, s82, v108
	v_med3_f32 v65, v57, s82, v108
	v_med3_f32 v66, v58, s82, v108
	v_med3_f32 v67, v59, s82, v108
	v_med3_f32 v68, v60, s82, v108
	v_med3_f32 v69, v61, s82, v108
	v_cvt_pk_bf16_f32 v192, v54, v55
	v_cvt_pk_bf16_f32 v193, v56, v57
	v_cvt_pk_bf16_f32 v194, v58, v59
	v_cvt_pk_bf16_f32 v195, v60, v61
	v_cvt_pk_fp8_f32 v70, v62, v63
	v_cvt_pk_fp8_f32 v71, v66, v67
	v_cvt_pk_fp8_f32 v70, v64, v65 op_sel:[0,0,1]
	v_cvt_pk_fp8_f32 v71, v68, v69 op_sel:[0,0,1]
	s_nop 0
	global_store_dwordx2 v[72:73], v[70:71], off offset:128
	v_mfma_f32_32x32x16_bf16 v[2:17], v[192:195], v[116:119], v[2:17]
	v_mfma_f32_32x32x16_bf16 v[18:33], v[192:195], v[120:123], v[18:33]
	v_mfma_f32_32x32x16_bf16 v[2:17], v[192:195], v[124:127], v[2:17]
	v_mfma_f32_32x32x16_bf16 v[18:33], v[192:195], v[128:131], v[18:33]
	v_lshlrev_b32_e32 v252, 16, v192
	v_and_b32_e32 v253, 0xffff0000, v192
	v_sub_f32_e32 v62, v54, v252
	v_sub_f32_e32 v63, v55, v253
	v_lshlrev_b32_e32 v252, 16, v193
	v_and_b32_e32 v253, 0xffff0000, v193
	v_sub_f32_e32 v64, v56, v252
	v_sub_f32_e32 v65, v57, v253
	v_lshlrev_b32_e32 v252, 16, v194
	v_and_b32_e32 v253, 0xffff0000, v194
	v_sub_f32_e32 v66, v58, v252
	v_sub_f32_e32 v67, v59, v253
	v_lshlrev_b32_e32 v252, 16, v195
	v_and_b32_e32 v253, 0xffff0000, v195
	v_sub_f32_e32 v68, v60, v252
	v_sub_f32_e32 v69, v61, v253
	v_cvt_pk_bf16_f32 v248, v62, v63
	v_cvt_pk_bf16_f32 v249, v64, v65
	v_cvt_pk_bf16_f32 v250, v66, v67
	v_cvt_pk_bf16_f32 v251, v68, v69
	s_nop 1
	v_mfma_f32_32x32x16_bf16 v[2:17], v[248:251], v[116:119], v[2:17]
	v_mfma_f32_32x32x16_bf16 v[18:33], v[248:251], v[120:123], v[18:33]
	global_load_dwordx4 v[112:115], v[196:197], off offset:384
	v_lshl_add_u64 v[34:35], v[34:35], 0, v[198:199]
	v_lshl_add_u64 v[36:37], v[36:37], 0, v[198:199]
	v_lshl_add_u64 v[38:39], v[38:39], 0, v[198:199]
	v_lshl_add_u64 v[40:41], v[40:41], 0, v[198:199]
	global_load_dwordx4 v[116:119], v[34:35], off
	global_load_dwordx4 v[120:123], v[36:37], off
	global_load_dwordx4 v[124:127], v[38:39], off
	global_load_dwordx4 v[128:131], v[40:41], off
	s_waitcnt lgkmcnt(0)
	ds_read_b128 v[200:203], v111 offset:640
	ds_read_b128 v[204:207], v111 offset:656
	ds_read_b128 v[208:211], v111 offset:1664
	ds_read_b128 v[212:215], v111 offset:1680
	ds_read_b128 v[216:219], v111 offset:2688
	ds_read_b128 v[220:223], v111 offset:2704
	s_waitcnt vmcnt(18)
	v_lshlrev_b32_e32 v54, 16, v132
	v_and_b32_e32 v55, 0xffff0000, v132
	v_lshlrev_b32_e32 v56, 16, v133
	v_and_b32_e32 v57, 0xffff0000, v133
	v_lshlrev_b32_e32 v58, 16, v134
	v_and_b32_e32 v59, 0xffff0000, v134
	v_lshlrev_b32_e32 v60, 16, v135
	v_and_b32_e32 v61, 0xffff0000, v135
	v_pk_mul_f32 v[54:55], v[46:47], v[54:55]
	v_pk_mul_f32 v[56:57], v[46:47], v[56:57]
	v_pk_mul_f32 v[58:59], v[46:47], v[58:59]
	v_pk_mul_f32 v[60:61], v[46:47], v[60:61]
	v_pk_mul_f32 v[54:55], v[224:225], v[54:55]
	v_pk_mul_f32 v[56:57], v[226:227], v[56:57]
	v_pk_mul_f32 v[58:59], v[228:229], v[58:59]
	v_pk_mul_f32 v[60:61], v[230:231], v[60:61]
	v_pk_fma_f32 v[54:55], v[232:233], v[54:55], v[240:241]
	v_pk_fma_f32 v[56:57], v[234:235], v[56:57], v[242:243]
	v_pk_fma_f32 v[58:59], v[236:237], v[58:59], v[244:245]
	v_pk_fma_f32 v[60:61], v[238:239], v[60:61], v[246:247]
	v_med3_f32 v62, v54, s82, v108
	v_med3_f32 v63, v55, s82, v108
	v_med3_f32 v64, v56, s82, v108
	v_med3_f32 v65, v57, s82, v108
	v_med3_f32 v66, v58, s82, v108
	v_med3_f32 v67, v59, s82, v108
	v_med3_f32 v68, v60, s82, v108
	v_med3_f32 v69, v61, s82, v108
	v_cvt_pk_bf16_f32 v192, v54, v55
	v_cvt_pk_bf16_f32 v193, v56, v57
	v_cvt_pk_bf16_f32 v194, v58, v59
	v_cvt_pk_bf16_f32 v195, v60, v61
	v_cvt_pk_fp8_f32 v70, v62, v63
	v_cvt_pk_fp8_f32 v71, v66, v67
	v_cvt_pk_fp8_f32 v70, v64, v65 op_sel:[0,0,1]
	v_cvt_pk_fp8_f32 v71, v68, v69 op_sel:[0,0,1]
	s_nop 0
	global_store_dwordx2 v[72:73], v[70:71], off offset:144
	v_mfma_f32_32x32x16_bf16 v[2:17], v[192:195], v[136:139], v[2:17]
	v_mfma_f32_32x32x16_bf16 v[18:33], v[192:195], v[140:143], v[18:33]
	v_mfma_f32_32x32x16_bf16 v[2:17], v[192:195], v[144:147], v[2:17]
	v_mfma_f32_32x32x16_bf16 v[18:33], v[192:195], v[148:151], v[18:33]
	v_lshlrev_b32_e32 v252, 16, v192
	v_and_b32_e32 v253, 0xffff0000, v192
	v_sub_f32_e32 v62, v54, v252
	v_sub_f32_e32 v63, v55, v253
	v_lshlrev_b32_e32 v252, 16, v193
	v_and_b32_e32 v253, 0xffff0000, v193
	v_sub_f32_e32 v64, v56, v252
	v_sub_f32_e32 v65, v57, v253
	v_lshlrev_b32_e32 v252, 16, v194
	v_and_b32_e32 v253, 0xffff0000, v194
	v_sub_f32_e32 v66, v58, v252
	v_sub_f32_e32 v67, v59, v253
	v_lshlrev_b32_e32 v252, 16, v195
	v_and_b32_e32 v253, 0xffff0000, v195
	v_sub_f32_e32 v68, v60, v252
	v_sub_f32_e32 v69, v61, v253
	v_cvt_pk_bf16_f32 v248, v62, v63
	v_cvt_pk_bf16_f32 v249, v64, v65
	v_cvt_pk_bf16_f32 v250, v66, v67
	v_cvt_pk_bf16_f32 v251, v68, v69
	s_nop 1
	v_mfma_f32_32x32x16_bf16 v[2:17], v[248:251], v[136:139], v[2:17]
	v_mfma_f32_32x32x16_bf16 v[18:33], v[248:251], v[140:143], v[18:33]
	global_load_dwordx4 v[132:135], v[196:197], off offset:416
	global_load_dwordx4 v[136:139], v[34:35], off offset:1024
	global_load_dwordx4 v[140:143], v[36:37], off offset:1024
	global_load_dwordx4 v[144:147], v[38:39], off offset:1024
	global_load_dwordx4 v[148:151], v[40:41], off offset:1024
	s_waitcnt lgkmcnt(0)
	ds_read_b128 v[224:227], v111 offset:704
	ds_read_b128 v[228:231], v111 offset:720
	ds_read_b128 v[232:235], v111 offset:1728
	ds_read_b128 v[236:239], v111 offset:1744
	ds_read_b128 v[240:243], v111 offset:2752
	ds_read_b128 v[244:247], v111 offset:2768
	s_waitcnt vmcnt(18)
	v_lshlrev_b32_e32 v54, 16, v152
	v_and_b32_e32 v55, 0xffff0000, v152
	v_lshlrev_b32_e32 v56, 16, v153
	v_and_b32_e32 v57, 0xffff0000, v153
	v_lshlrev_b32_e32 v58, 16, v154
	v_and_b32_e32 v59, 0xffff0000, v154
	v_lshlrev_b32_e32 v60, 16, v155
	v_and_b32_e32 v61, 0xffff0000, v155
	v_pk_mul_f32 v[54:55], v[46:47], v[54:55]
	v_pk_mul_f32 v[56:57], v[46:47], v[56:57]
	v_pk_mul_f32 v[58:59], v[46:47], v[58:59]
	v_pk_mul_f32 v[60:61], v[46:47], v[60:61]
	v_pk_mul_f32 v[54:55], v[200:201], v[54:55]
	v_pk_mul_f32 v[56:57], v[202:203], v[56:57]
	v_pk_mul_f32 v[58:59], v[204:205], v[58:59]
	v_pk_mul_f32 v[60:61], v[206:207], v[60:61]
	v_pk_fma_f32 v[54:55], v[208:209], v[54:55], v[216:217]
	v_pk_fma_f32 v[56:57], v[210:211], v[56:57], v[218:219]
	v_pk_fma_f32 v[58:59], v[212:213], v[58:59], v[220:221]
	v_pk_fma_f32 v[60:61], v[214:215], v[60:61], v[222:223]
	v_med3_f32 v62, v54, s82, v108
	v_med3_f32 v63, v55, s82, v108
	v_med3_f32 v64, v56, s82, v108
	v_med3_f32 v65, v57, s82, v108
	v_med3_f32 v66, v58, s82, v108
	v_med3_f32 v67, v59, s82, v108
	v_med3_f32 v68, v60, s82, v108
	v_med3_f32 v69, v61, s82, v108
	v_cvt_pk_bf16_f32 v192, v54, v55
	v_cvt_pk_bf16_f32 v193, v56, v57
	v_cvt_pk_bf16_f32 v194, v58, v59
	v_cvt_pk_bf16_f32 v195, v60, v61
	v_cvt_pk_fp8_f32 v70, v62, v63
	v_cvt_pk_fp8_f32 v71, v66, v67
	v_cvt_pk_fp8_f32 v70, v64, v65 op_sel:[0,0,1]
	v_cvt_pk_fp8_f32 v71, v68, v69 op_sel:[0,0,1]
	s_nop 0
	global_store_dwordx2 v[72:73], v[70:71], off offset:160
	v_mfma_f32_32x32x16_bf16 v[2:17], v[192:195], v[156:159], v[2:17]
	v_mfma_f32_32x32x16_bf16 v[18:33], v[192:195], v[160:163], v[18:33]
	v_mfma_f32_32x32x16_bf16 v[2:17], v[192:195], v[164:167], v[2:17]
	v_mfma_f32_32x32x16_bf16 v[18:33], v[192:195], v[168:171], v[18:33]
	v_lshlrev_b32_e32 v252, 16, v192
	v_and_b32_e32 v253, 0xffff0000, v192
	v_sub_f32_e32 v62, v54, v252
	v_sub_f32_e32 v63, v55, v253
	v_lshlrev_b32_e32 v252, 16, v193
	v_and_b32_e32 v253, 0xffff0000, v193
	v_sub_f32_e32 v64, v56, v252
	v_sub_f32_e32 v65, v57, v253
	v_lshlrev_b32_e32 v252, 16, v194
	v_and_b32_e32 v253, 0xffff0000, v194
	v_sub_f32_e32 v66, v58, v252
	v_sub_f32_e32 v67, v59, v253
	v_lshlrev_b32_e32 v252, 16, v195
	v_and_b32_e32 v253, 0xffff0000, v195
	v_sub_f32_e32 v68, v60, v252
	v_sub_f32_e32 v69, v61, v253
	v_cvt_pk_bf16_f32 v248, v62, v63
	v_cvt_pk_bf16_f32 v249, v64, v65
	v_cvt_pk_bf16_f32 v250, v66, v67
	v_cvt_pk_bf16_f32 v251, v68, v69
	s_nop 1
	v_mfma_f32_32x32x16_bf16 v[2:17], v[248:251], v[156:159], v[2:17]
	v_mfma_f32_32x32x16_bf16 v[18:33], v[248:251], v[160:163], v[18:33]
	global_load_dwordx4 v[152:155], v[196:197], off offset:448
	global_load_dwordx4 v[156:159], v[34:35], off offset:2048
	global_load_dwordx4 v[160:163], v[36:37], off offset:2048
	global_load_dwordx4 v[164:167], v[38:39], off offset:2048
	global_load_dwordx4 v[168:171], v[40:41], off offset:2048
	s_waitcnt lgkmcnt(0)
	ds_read_b128 v[200:203], v111 offset:768
	ds_read_b128 v[204:207], v111 offset:784
	ds_read_b128 v[208:211], v111 offset:1792
	ds_read_b128 v[212:215], v111 offset:1808
	ds_read_b128 v[216:219], v111 offset:2816
	ds_read_b128 v[220:223], v111 offset:2832
	s_waitcnt vmcnt(18)
	v_lshlrev_b32_e32 v54, 16, v172
	v_and_b32_e32 v55, 0xffff0000, v172
	v_lshlrev_b32_e32 v56, 16, v173
	v_and_b32_e32 v57, 0xffff0000, v173
	v_lshlrev_b32_e32 v58, 16, v174
	v_and_b32_e32 v59, 0xffff0000, v174
	v_lshlrev_b32_e32 v60, 16, v175
	v_and_b32_e32 v61, 0xffff0000, v175
	v_pk_mul_f32 v[54:55], v[46:47], v[54:55]
	v_pk_mul_f32 v[56:57], v[46:47], v[56:57]
	v_pk_mul_f32 v[58:59], v[46:47], v[58:59]
	v_pk_mul_f32 v[60:61], v[46:47], v[60:61]
	v_pk_mul_f32 v[54:55], v[224:225], v[54:55]
	v_pk_mul_f32 v[56:57], v[226:227], v[56:57]
	v_pk_mul_f32 v[58:59], v[228:229], v[58:59]
	v_pk_mul_f32 v[60:61], v[230:231], v[60:61]
	v_pk_fma_f32 v[54:55], v[232:233], v[54:55], v[240:241]
	v_pk_fma_f32 v[56:57], v[234:235], v[56:57], v[242:243]
	v_pk_fma_f32 v[58:59], v[236:237], v[58:59], v[244:245]
	v_pk_fma_f32 v[60:61], v[238:239], v[60:61], v[246:247]
	v_med3_f32 v62, v54, s82, v108
	v_med3_f32 v63, v55, s82, v108
	v_med3_f32 v64, v56, s82, v108
	v_med3_f32 v65, v57, s82, v108
	v_med3_f32 v66, v58, s82, v108
	v_med3_f32 v67, v59, s82, v108
	v_med3_f32 v68, v60, s82, v108
	v_med3_f32 v69, v61, s82, v108
	v_cvt_pk_bf16_f32 v192, v54, v55
	v_cvt_pk_bf16_f32 v193, v56, v57
	v_cvt_pk_bf16_f32 v194, v58, v59
	v_cvt_pk_bf16_f32 v195, v60, v61
	v_cvt_pk_fp8_f32 v70, v62, v63
	v_cvt_pk_fp8_f32 v71, v66, v67
	v_cvt_pk_fp8_f32 v70, v64, v65 op_sel:[0,0,1]
	v_cvt_pk_fp8_f32 v71, v68, v69 op_sel:[0,0,1]
	s_nop 0
	global_store_dwordx2 v[72:73], v[70:71], off offset:176
	v_mfma_f32_32x32x16_bf16 v[2:17], v[192:195], v[176:179], v[2:17]
	v_mfma_f32_32x32x16_bf16 v[18:33], v[192:195], v[180:183], v[18:33]
	v_mfma_f32_32x32x16_bf16 v[2:17], v[192:195], v[184:187], v[2:17]
	v_mfma_f32_32x32x16_bf16 v[18:33], v[192:195], v[188:191], v[18:33]
	v_lshlrev_b32_e32 v252, 16, v192
	v_and_b32_e32 v253, 0xffff0000, v192
	v_sub_f32_e32 v62, v54, v252
	v_sub_f32_e32 v63, v55, v253
	v_lshlrev_b32_e32 v252, 16, v193
	v_and_b32_e32 v253, 0xffff0000, v193
	v_sub_f32_e32 v64, v56, v252
	v_sub_f32_e32 v65, v57, v253
	v_lshlrev_b32_e32 v252, 16, v194
	v_and_b32_e32 v253, 0xffff0000, v194
	v_sub_f32_e32 v66, v58, v252
	v_sub_f32_e32 v67, v59, v253
	v_lshlrev_b32_e32 v252, 16, v195
	v_and_b32_e32 v253, 0xffff0000, v195
	v_sub_f32_e32 v68, v60, v252
	v_sub_f32_e32 v69, v61, v253
	v_cvt_pk_bf16_f32 v248, v62, v63
	v_cvt_pk_bf16_f32 v249, v64, v65
	v_cvt_pk_bf16_f32 v250, v66, v67
	v_cvt_pk_bf16_f32 v251, v68, v69
	s_nop 1
	v_mfma_f32_32x32x16_bf16 v[2:17], v[248:251], v[176:179], v[2:17]
	v_mfma_f32_32x32x16_bf16 v[18:33], v[248:251], v[180:183], v[18:33]
	global_load_dwordx4 v[172:175], v[196:197], off offset:480
	global_load_dwordx4 v[176:179], v[34:35], off offset:3072
	global_load_dwordx4 v[180:183], v[36:37], off offset:3072
	global_load_dwordx4 v[184:187], v[38:39], off offset:3072
	global_load_dwordx4 v[188:191], v[40:41], off offset:3072
	s_waitcnt lgkmcnt(0)
	ds_read_b128 v[224:227], v111 offset:832
	ds_read_b128 v[228:231], v111 offset:848
	ds_read_b128 v[232:235], v111 offset:1856
	ds_read_b128 v[236:239], v111 offset:1872
	ds_read_b128 v[240:243], v111 offset:2880
	ds_read_b128 v[244:247], v111 offset:2896
	s_waitcnt vmcnt(18)
	v_lshlrev_b32_e32 v54, 16, v112
	v_and_b32_e32 v55, 0xffff0000, v112
	v_lshlrev_b32_e32 v56, 16, v113
	v_and_b32_e32 v57, 0xffff0000, v113
	v_lshlrev_b32_e32 v58, 16, v114
	v_and_b32_e32 v59, 0xffff0000, v114
	v_lshlrev_b32_e32 v60, 16, v115
	v_and_b32_e32 v61, 0xffff0000, v115
	v_pk_mul_f32 v[54:55], v[46:47], v[54:55]
	v_pk_mul_f32 v[56:57], v[46:47], v[56:57]
	v_pk_mul_f32 v[58:59], v[46:47], v[58:59]
	v_pk_mul_f32 v[60:61], v[46:47], v[60:61]
	v_pk_mul_f32 v[54:55], v[200:201], v[54:55]
	v_pk_mul_f32 v[56:57], v[202:203], v[56:57]
	v_pk_mul_f32 v[58:59], v[204:205], v[58:59]
	v_pk_mul_f32 v[60:61], v[206:207], v[60:61]
	v_pk_fma_f32 v[54:55], v[208:209], v[54:55], v[216:217]
	v_pk_fma_f32 v[56:57], v[210:211], v[56:57], v[218:219]
	v_pk_fma_f32 v[58:59], v[212:213], v[58:59], v[220:221]
	v_pk_fma_f32 v[60:61], v[214:215], v[60:61], v[222:223]
	v_med3_f32 v62, v54, s82, v108
	v_med3_f32 v63, v55, s82, v108
	v_med3_f32 v64, v56, s82, v108
	v_med3_f32 v65, v57, s82, v108
	v_med3_f32 v66, v58, s82, v108
	v_med3_f32 v67, v59, s82, v108
	v_med3_f32 v68, v60, s82, v108
	v_med3_f32 v69, v61, s82, v108
	v_cvt_pk_bf16_f32 v192, v54, v55
	v_cvt_pk_bf16_f32 v193, v56, v57
	v_cvt_pk_bf16_f32 v194, v58, v59
	v_cvt_pk_bf16_f32 v195, v60, v61
	v_cvt_pk_fp8_f32 v70, v62, v63
	v_cvt_pk_fp8_f32 v71, v66, v67
	v_cvt_pk_fp8_f32 v70, v64, v65 op_sel:[0,0,1]
	v_cvt_pk_fp8_f32 v71, v68, v69 op_sel:[0,0,1]
	s_nop 0
	global_store_dwordx2 v[72:73], v[70:71], off offset:192
	v_mfma_f32_32x32x16_bf16 v[2:17], v[192:195], v[116:119], v[2:17]
	v_mfma_f32_32x32x16_bf16 v[18:33], v[192:195], v[120:123], v[18:33]
	v_mfma_f32_32x32x16_bf16 v[2:17], v[192:195], v[124:127], v[2:17]
	v_mfma_f32_32x32x16_bf16 v[18:33], v[192:195], v[128:131], v[18:33]
	v_lshlrev_b32_e32 v252, 16, v192
	v_and_b32_e32 v253, 0xffff0000, v192
	v_sub_f32_e32 v62, v54, v252
	v_sub_f32_e32 v63, v55, v253
	v_lshlrev_b32_e32 v252, 16, v193
	v_and_b32_e32 v253, 0xffff0000, v193
	v_sub_f32_e32 v64, v56, v252
	v_sub_f32_e32 v65, v57, v253
	v_lshlrev_b32_e32 v252, 16, v194
	v_and_b32_e32 v253, 0xffff0000, v194
	v_sub_f32_e32 v66, v58, v252
	v_sub_f32_e32 v67, v59, v253
	v_lshlrev_b32_e32 v252, 16, v195
	v_and_b32_e32 v253, 0xffff0000, v195
	v_sub_f32_e32 v68, v60, v252
	v_sub_f32_e32 v69, v61, v253
	v_cvt_pk_bf16_f32 v248, v62, v63
	v_cvt_pk_bf16_f32 v249, v64, v65
	v_cvt_pk_bf16_f32 v250, v66, v67
	v_cvt_pk_bf16_f32 v251, v68, v69
	s_nop 1
	v_mfma_f32_32x32x16_bf16 v[2:17], v[248:251], v[116:119], v[2:17]
	v_mfma_f32_32x32x16_bf16 v[18:33], v[248:251], v[120:123], v[18:33]
	s_waitcnt lgkmcnt(0)
	ds_read_b128 v[200:203], v111 offset:896
	ds_read_b128 v[204:207], v111 offset:912
	ds_read_b128 v[208:211], v111 offset:1920
	ds_read_b128 v[212:215], v111 offset:1936
	ds_read_b128 v[216:219], v111 offset:2944
	ds_read_b128 v[220:223], v111 offset:2960
	s_waitcnt vmcnt(13)
	v_lshlrev_b32_e32 v54, 16, v132
	v_and_b32_e32 v55, 0xffff0000, v132
	v_lshlrev_b32_e32 v56, 16, v133
	v_and_b32_e32 v57, 0xffff0000, v133
	v_lshlrev_b32_e32 v58, 16, v134
	v_and_b32_e32 v59, 0xffff0000, v134
	v_lshlrev_b32_e32 v60, 16, v135
	v_and_b32_e32 v61, 0xffff0000, v135
	v_pk_mul_f32 v[54:55], v[46:47], v[54:55]
	v_pk_mul_f32 v[56:57], v[46:47], v[56:57]
	v_pk_mul_f32 v[58:59], v[46:47], v[58:59]
	v_pk_mul_f32 v[60:61], v[46:47], v[60:61]
	v_pk_mul_f32 v[54:55], v[224:225], v[54:55]
	v_pk_mul_f32 v[56:57], v[226:227], v[56:57]
	v_pk_mul_f32 v[58:59], v[228:229], v[58:59]
	v_pk_mul_f32 v[60:61], v[230:231], v[60:61]
	v_pk_fma_f32 v[54:55], v[232:233], v[54:55], v[240:241]
	v_pk_fma_f32 v[56:57], v[234:235], v[56:57], v[242:243]
	v_pk_fma_f32 v[58:59], v[236:237], v[58:59], v[244:245]
	v_pk_fma_f32 v[60:61], v[238:239], v[60:61], v[246:247]
	v_med3_f32 v62, v54, s82, v108
	v_med3_f32 v63, v55, s82, v108
	v_med3_f32 v64, v56, s82, v108
	v_med3_f32 v65, v57, s82, v108
	v_med3_f32 v66, v58, s82, v108
	v_med3_f32 v67, v59, s82, v108
	v_med3_f32 v68, v60, s82, v108
	v_med3_f32 v69, v61, s82, v108
	v_cvt_pk_bf16_f32 v192, v54, v55
	v_cvt_pk_bf16_f32 v193, v56, v57
	v_cvt_pk_bf16_f32 v194, v58, v59
	v_cvt_pk_bf16_f32 v195, v60, v61
	v_cvt_pk_fp8_f32 v70, v62, v63
	v_cvt_pk_fp8_f32 v71, v66, v67
	v_cvt_pk_fp8_f32 v70, v64, v65 op_sel:[0,0,1]
	v_cvt_pk_fp8_f32 v71, v68, v69 op_sel:[0,0,1]
	s_nop 0
	global_store_dwordx2 v[72:73], v[70:71], off offset:208
	v_mfma_f32_32x32x16_bf16 v[2:17], v[192:195], v[136:139], v[2:17]
	v_mfma_f32_32x32x16_bf16 v[18:33], v[192:195], v[140:143], v[18:33]
	v_mfma_f32_32x32x16_bf16 v[2:17], v[192:195], v[144:147], v[2:17]
	v_mfma_f32_32x32x16_bf16 v[18:33], v[192:195], v[148:151], v[18:33]
	v_lshlrev_b32_e32 v252, 16, v192
	v_and_b32_e32 v253, 0xffff0000, v192
	v_sub_f32_e32 v62, v54, v252
	v_sub_f32_e32 v63, v55, v253
	v_lshlrev_b32_e32 v252, 16, v193
	v_and_b32_e32 v253, 0xffff0000, v193
	v_sub_f32_e32 v64, v56, v252
	v_sub_f32_e32 v65, v57, v253
	v_lshlrev_b32_e32 v252, 16, v194
	v_and_b32_e32 v253, 0xffff0000, v194
	v_sub_f32_e32 v66, v58, v252
	v_sub_f32_e32 v67, v59, v253
	v_lshlrev_b32_e32 v252, 16, v195
	v_and_b32_e32 v253, 0xffff0000, v195
	v_sub_f32_e32 v68, v60, v252
	v_sub_f32_e32 v69, v61, v253
	v_cvt_pk_bf16_f32 v248, v62, v63
	v_cvt_pk_bf16_f32 v249, v64, v65
	v_cvt_pk_bf16_f32 v250, v66, v67
	v_cvt_pk_bf16_f32 v251, v68, v69
	s_nop 1
	v_mfma_f32_32x32x16_bf16 v[2:17], v[248:251], v[136:139], v[2:17]
	v_mfma_f32_32x32x16_bf16 v[18:33], v[248:251], v[140:143], v[18:33]
	s_waitcnt lgkmcnt(0)
	ds_read_b128 v[224:227], v111 offset:960
	ds_read_b128 v[228:231], v111 offset:976
	ds_read_b128 v[232:235], v111 offset:1984
	ds_read_b128 v[236:239], v111 offset:2000
	ds_read_b128 v[240:243], v111 offset:3008
	ds_read_b128 v[244:247], v111 offset:3024
	s_waitcnt vmcnt(8)
	v_lshlrev_b32_e32 v54, 16, v152
	v_and_b32_e32 v55, 0xffff0000, v152
	v_lshlrev_b32_e32 v56, 16, v153
	v_and_b32_e32 v57, 0xffff0000, v153
	v_lshlrev_b32_e32 v58, 16, v154
	v_and_b32_e32 v59, 0xffff0000, v154
	v_lshlrev_b32_e32 v60, 16, v155
	v_and_b32_e32 v61, 0xffff0000, v155
	v_pk_mul_f32 v[54:55], v[46:47], v[54:55]
	v_pk_mul_f32 v[56:57], v[46:47], v[56:57]
	v_pk_mul_f32 v[58:59], v[46:47], v[58:59]
	v_pk_mul_f32 v[60:61], v[46:47], v[60:61]
	v_pk_mul_f32 v[54:55], v[200:201], v[54:55]
	v_pk_mul_f32 v[56:57], v[202:203], v[56:57]
	v_pk_mul_f32 v[58:59], v[204:205], v[58:59]
	v_pk_mul_f32 v[60:61], v[206:207], v[60:61]
	v_pk_fma_f32 v[54:55], v[208:209], v[54:55], v[216:217]
	v_pk_fma_f32 v[56:57], v[210:211], v[56:57], v[218:219]
	v_pk_fma_f32 v[58:59], v[212:213], v[58:59], v[220:221]
	v_pk_fma_f32 v[60:61], v[214:215], v[60:61], v[222:223]
	v_med3_f32 v62, v54, s82, v108
	v_med3_f32 v63, v55, s82, v108
	v_med3_f32 v64, v56, s82, v108
	v_med3_f32 v65, v57, s82, v108
	v_med3_f32 v66, v58, s82, v108
	v_med3_f32 v67, v59, s82, v108
	v_med3_f32 v68, v60, s82, v108
	v_med3_f32 v69, v61, s82, v108
	v_cvt_pk_bf16_f32 v192, v54, v55
	v_cvt_pk_bf16_f32 v193, v56, v57
	v_cvt_pk_bf16_f32 v194, v58, v59
	v_cvt_pk_bf16_f32 v195, v60, v61
	v_cvt_pk_fp8_f32 v70, v62, v63
	v_cvt_pk_fp8_f32 v71, v66, v67
	v_cvt_pk_fp8_f32 v70, v64, v65 op_sel:[0,0,1]
	v_cvt_pk_fp8_f32 v71, v68, v69 op_sel:[0,0,1]
	s_nop 0
	global_store_dwordx2 v[72:73], v[70:71], off offset:224
	v_mfma_f32_32x32x16_bf16 v[2:17], v[192:195], v[156:159], v[2:17]
	v_mfma_f32_32x32x16_bf16 v[18:33], v[192:195], v[160:163], v[18:33]
	v_mfma_f32_32x32x16_bf16 v[2:17], v[192:195], v[164:167], v[2:17]
	v_mfma_f32_32x32x16_bf16 v[18:33], v[192:195], v[168:171], v[18:33]
	v_lshlrev_b32_e32 v252, 16, v192
	v_and_b32_e32 v253, 0xffff0000, v192
	v_sub_f32_e32 v62, v54, v252
	v_sub_f32_e32 v63, v55, v253
	v_lshlrev_b32_e32 v252, 16, v193
	v_and_b32_e32 v253, 0xffff0000, v193
	v_sub_f32_e32 v64, v56, v252
	v_sub_f32_e32 v65, v57, v253
	v_lshlrev_b32_e32 v252, 16, v194
	v_and_b32_e32 v253, 0xffff0000, v194
	v_sub_f32_e32 v66, v58, v252
	v_sub_f32_e32 v67, v59, v253
	v_lshlrev_b32_e32 v252, 16, v195
	v_and_b32_e32 v253, 0xffff0000, v195
	v_sub_f32_e32 v68, v60, v252
	v_sub_f32_e32 v69, v61, v253
	v_cvt_pk_bf16_f32 v248, v62, v63
	v_cvt_pk_bf16_f32 v249, v64, v65
	v_cvt_pk_bf16_f32 v250, v66, v67
	v_cvt_pk_bf16_f32 v251, v68, v69
	s_nop 1
	v_mfma_f32_32x32x16_bf16 v[2:17], v[248:251], v[156:159], v[2:17]
	v_mfma_f32_32x32x16_bf16 v[18:33], v[248:251], v[160:163], v[18:33]
	s_waitcnt lgkmcnt(0)
	s_waitcnt vmcnt(3)
	v_lshlrev_b32_e32 v54, 16, v172
	v_and_b32_e32 v55, 0xffff0000, v172
	v_lshlrev_b32_e32 v56, 16, v173
	v_and_b32_e32 v57, 0xffff0000, v173
	v_lshlrev_b32_e32 v58, 16, v174
	v_and_b32_e32 v59, 0xffff0000, v174
	v_lshlrev_b32_e32 v60, 16, v175
	v_and_b32_e32 v61, 0xffff0000, v175
	v_pk_mul_f32 v[54:55], v[46:47], v[54:55]
	v_pk_mul_f32 v[56:57], v[46:47], v[56:57]
	v_pk_mul_f32 v[58:59], v[46:47], v[58:59]
	v_pk_mul_f32 v[60:61], v[46:47], v[60:61]
	v_pk_mul_f32 v[54:55], v[224:225], v[54:55]
	v_pk_mul_f32 v[56:57], v[226:227], v[56:57]
	v_pk_mul_f32 v[58:59], v[228:229], v[58:59]
	v_pk_mul_f32 v[60:61], v[230:231], v[60:61]
	v_pk_fma_f32 v[54:55], v[232:233], v[54:55], v[240:241]
	v_pk_fma_f32 v[56:57], v[234:235], v[56:57], v[242:243]
	v_pk_fma_f32 v[58:59], v[236:237], v[58:59], v[244:245]
	v_pk_fma_f32 v[60:61], v[238:239], v[60:61], v[246:247]
	v_med3_f32 v62, v54, s82, v108
	v_med3_f32 v63, v55, s82, v108
	v_med3_f32 v64, v56, s82, v108
	v_med3_f32 v65, v57, s82, v108
	v_med3_f32 v66, v58, s82, v108
	v_med3_f32 v67, v59, s82, v108
	v_med3_f32 v68, v60, s82, v108
	v_med3_f32 v69, v61, s82, v108
	v_cvt_pk_bf16_f32 v192, v54, v55
	v_cvt_pk_bf16_f32 v193, v56, v57
	v_cvt_pk_bf16_f32 v194, v58, v59
	v_cvt_pk_bf16_f32 v195, v60, v61
	v_cvt_pk_fp8_f32 v70, v62, v63
	v_cvt_pk_fp8_f32 v71, v66, v67
	v_cvt_pk_fp8_f32 v70, v64, v65 op_sel:[0,0,1]
	v_cvt_pk_fp8_f32 v71, v68, v69 op_sel:[0,0,1]
	s_nop 0
	global_store_dwordx2 v[72:73], v[70:71], off offset:240
	v_mfma_f32_32x32x16_bf16 v[2:17], v[192:195], v[176:179], v[2:17]
	v_mfma_f32_32x32x16_bf16 v[18:33], v[192:195], v[180:183], v[18:33]
	v_mfma_f32_32x32x16_bf16 v[2:17], v[192:195], v[184:187], v[2:17]
	v_mfma_f32_32x32x16_bf16 v[18:33], v[192:195], v[188:191], v[18:33]
	v_lshlrev_b32_e32 v252, 16, v192
	v_and_b32_e32 v253, 0xffff0000, v192
	v_sub_f32_e32 v62, v54, v252
	v_sub_f32_e32 v63, v55, v253
	v_lshlrev_b32_e32 v252, 16, v193
	v_and_b32_e32 v253, 0xffff0000, v193
	v_sub_f32_e32 v64, v56, v252
	v_sub_f32_e32 v65, v57, v253
	v_lshlrev_b32_e32 v252, 16, v194
	v_and_b32_e32 v253, 0xffff0000, v194
	v_sub_f32_e32 v66, v58, v252
	v_sub_f32_e32 v67, v59, v253
	v_lshlrev_b32_e32 v252, 16, v195
	v_and_b32_e32 v253, 0xffff0000, v195
	v_sub_f32_e32 v68, v60, v252
	v_sub_f32_e32 v69, v61, v253
	v_cvt_pk_bf16_f32 v248, v62, v63
	v_cvt_pk_bf16_f32 v249, v64, v65
	v_cvt_pk_bf16_f32 v250, v66, v67
	v_cvt_pk_bf16_f32 v251, v68, v69
	s_nop 1
	v_mfma_f32_32x32x16_bf16 v[2:17], v[248:251], v[176:179], v[2:17]
	v_mfma_f32_32x32x16_bf16 v[18:33], v[248:251], v[180:183], v[18:33]
	v_and_b32_e32 v62, 0xffffff00, v103
	v_lshlrev_b32_e32 v62, 6, v62
	v_lshl_add_u32 v62, v254, 4, v62
	v_lshlrev_b32_e32 v63, 12, v75
	v_sub_u32_e32 v62, v62, v63
	v_add_u32_e32 v62, 0x3000, v62
	v_sub_u32_e32 v62, 0, v62
	v_ashrrev_i32_e32 v63, 31, v62
	v_lshl_add_u64 v[34:35], v[34:35], 0, v[62:63]
	v_lshl_add_u64 v[36:37], v[36:37], 0, v[62:63]
	v_lshl_add_u64 v[38:39], v[38:39], 0, v[62:63]
	v_lshl_add_u64 v[40:41], v[40:41], 0, v[62:63]
	s_nop 7
	v_add_u32_e32 v1, 0x400, v83
	s_nop 9
	ds_write2_b32 v1, v2, v18 offset1:32
	ds_write2_b32 v1, v3, v19 offset0:64 offset1:96
	ds_write2_b32 v1, v4, v20 offset0:128 offset1:160
	ds_write2_b32 v1, v5, v21 offset0:192 offset1:224
	v_add_u32_e32 v1, 0xc00, v83
	ds_write2_b32 v1, v6, v22 offset1:32
	ds_write2_b32 v1, v7, v23 offset0:64 offset1:96
	ds_write2_b32 v1, v8, v24 offset0:128 offset1:160
	ds_write2_b32 v1, v9, v25 offset0:192 offset1:224
	v_add_u32_e32 v1, 0x1400, v83
	ds_write2_b32 v1, v10, v26 offset1:32
	ds_write2_b32 v1, v11, v27 offset0:64 offset1:96
	ds_write2_b32 v1, v12, v28 offset0:128 offset1:160
	ds_write2_b32 v1, v13, v29 offset0:192 offset1:224
	v_add_u32_e32 v1, 0x1c00, v83
	ds_write2_b32 v1, v14, v30 offset1:32
	ds_write2_b32 v1, v15, v31 offset0:64 offset1:96
	ds_write2_b32 v1, v16, v32 offset0:128 offset1:160
	ds_write2_b32 v1, v17, v33 offset0:192 offset1:224
	s_waitcnt lgkmcnt(0)
	s_barrier
	global_load_dword v1, v[42:43], off
	v_add_u32_e32 v8, s66, v84
	ds_read2st64_b32 v[2:3], v8 offset0:4 offset1:36
	ds_read2st64_b32 v[4:5], v8 offset0:68 offset1:100
	ds_read2st64_b32 v[6:7], v8 offset0:132 offset1:164
	ds_read2st64_b32 v[8:9], v8 offset0:196 offset1:228
	s_waitcnt lgkmcnt(3)
	v_add_f32_e32 v2, 0, v2
	v_add_f32_e32 v2, v2, v3
	s_waitcnt lgkmcnt(2)
	v_add_f32_e32 v2, v2, v4
	v_add_f32_e32 v2, v2, v5
	s_waitcnt lgkmcnt(1)
	v_add_f32_e32 v2, v2, v6
	v_add_f32_e32 v2, v2, v7
	s_waitcnt lgkmcnt(0)
	v_add_f32_e32 v2, v2, v8
	v_add_f32_e32 v2, v2, v9
	v_mul_f32_e32 v3, 0xbfb8aa3b, v2
	v_fma_f32 v4, v2, s83, -v3
	v_rndne_f32_e32 v5, v3
	v_fmac_f32_e32 v4, 0xb2a5705f, v2
	v_sub_f32_e32 v3, v3, v5
	v_add_f32_e32 v3, v3, v4
	v_cvt_i32_f32_e32 v5, v5
	v_exp_f32_e32 v3, v3
	v_cmp_nlt_f32_e32 vcc, s84, v2
	v_ldexp_f32 v3, v3, v5
	s_nop 0
	v_cndmask_b32_e32 v3, 0, v3, vcc
	v_cmp_ngt_f32_e32 vcc, s85, v2
	s_nop 1
	v_cndmask_b32_e32 v2, v109, v3, vcc
	v_add_f32_e32 v2, 1.0, v2
	v_div_scale_f32 v3, s[34:35], v2, v2, 1.0
	v_rcp_f32_e32 v4, v3
	v_div_scale_f32 v5, vcc, 1.0, v2, 1.0
	v_fma_f32 v6, -v3, v4, 1.0
	v_fmac_f32_e32 v4, v6, v4
	v_mul_f32_e32 v6, v5, v4
	v_fma_f32 v7, -v3, v6, v5
	v_fmac_f32_e32 v6, v7, v4
	v_fma_f32 v3, -v3, v6, v5
	v_div_fmas_f32 v3, v3, v4, v6
	v_div_fixup_f32 v2, v3, v2, 1.0
	s_waitcnt vmcnt(0)
	v_mov_b32_e32 v128, v1
	v_add_f32_e32 v1, v1, v2
	ds_bpermute_b32 v3, v88, v1
	ds_bpermute_b32 v4, v89, v1
	ds_bpermute_b32 v5, v90, v1
	ds_bpermute_b32 v6, v91, v1
	ds_bpermute_b32 v7, v92, v1
	s_waitcnt lgkmcnt(4)
	v_cmp_eq_f32_e64 s[34:35], v1, v3
	v_cmp_lt_f32_e32 vcc, v1, v3
	s_waitcnt lgkmcnt(3)
	v_cmp_eq_f32_e64 s[38:39], v1, v4
	s_and_b64 s[34:35], s[4:5], s[34:35]
	v_cmp_lt_f32_e64 s[36:37], v1, v4
	s_waitcnt lgkmcnt(2)
	v_cmp_eq_f32_e64 s[42:43], v1, v5
	s_and_b64 s[38:39], s[6:7], s[38:39]
	s_or_b64 s[34:35], vcc, s[34:35]
	v_cmp_lt_f32_e64 s[40:41], v1, v5
	s_waitcnt lgkmcnt(1)
	v_cmp_eq_f32_e64 s[46:47], v1, v6
	s_and_b64 s[42:43], s[8:9], s[42:43]
	v_cndmask_b32_e64 v3, 0, 1, s[34:35]
	s_or_b64 s[34:35], s[36:37], s[38:39]
	v_cmp_lt_f32_e64 s[44:45], v1, v6
	s_and_b64 s[46:47], s[10:11], s[46:47]
	v_cndmask_b32_e64 v4, 0, 1, s[34:35]
	s_or_b64 s[34:35], s[40:41], s[42:43]
	v_cndmask_b32_e64 v5, 0, 1, s[34:35]
	s_or_b64 s[34:35], s[44:45], s[46:47]
	v_add3_u32 v3, v3, v4, v5
	v_cndmask_b32_e64 v4, 0, 1, s[34:35]
	s_waitcnt lgkmcnt(0)
	v_cmp_eq_f32_e64 s[34:35], v1, v7
	v_cmp_lt_f32_e32 vcc, v1, v7
	ds_bpermute_b32 v5, v93, v1
	s_and_b64 s[34:35], s[12:13], s[34:35]
	s_or_b64 s[34:35], vcc, s[34:35]
	v_cndmask_b32_e64 v6, 0, 1, s[34:35]
	v_add3_u32 v3, v3, v4, v6
	ds_bpermute_b32 v4, v94, v1
	s_waitcnt lgkmcnt(1)
	v_cmp_eq_f32_e64 s[34:35], v1, v5
	ds_bpermute_b32 v6, v95, v1
	v_cmp_lt_f32_e32 vcc, v1, v5
	s_and_b64 s[34:35], s[14:15], s[34:35]
	s_or_b64 s[34:35], vcc, s[34:35]
	v_cndmask_b32_e64 v5, 0, 1, s[34:35]
	s_waitcnt lgkmcnt(1)
	v_cmp_eq_f32_e64 s[34:35], v1, v4
	v_cmp_lt_f32_e32 vcc, v1, v4
	s_and_b64 s[34:35], s[16:17], s[34:35]
	s_or_b64 s[34:35], vcc, s[34:35]
	s_waitcnt lgkmcnt(0)
	v_cmp_lt_f32_e32 vcc, v1, v6
	v_cndmask_b32_e64 v4, 0, 1, s[34:35]
	s_mov_b32 s40, 0
	v_addc_co_u32_e32 v3, vcc, v3, v5, vcc
	v_add_u32_e32 v3, v3, v4
	v_cmp_gt_u32_e32 vcc, 2, v3
	s_nop 1
	v_cndmask_b32_e32 v3, 0, v1, vcc
	ds_bpermute_b32 v4, v76, v3
	s_waitcnt lgkmcnt(0)
	v_add_f32_e32 v3, v3, v4
	ds_bpermute_b32 v4, v77, v3
	s_waitcnt lgkmcnt(0)
	v_add_f32_e32 v3, v3, v4
	ds_bpermute_b32 v4, v78, v3
	s_waitcnt lgkmcnt(0)
	v_add_f32_e32 v3, v3, v4
	ds_bpermute_b32 v4, v87, v3
	ds_bpermute_b32 v5, v96, v3
	ds_bpermute_b32 v6, v97, v3
	ds_bpermute_b32 v7, v98, v3
	ds_bpermute_b32 v8, v99, v3
	s_waitcnt lgkmcnt(4)
	v_cmp_eq_f32_e64 s[34:35], v3, v4
	v_cmp_lt_f32_e32 vcc, v3, v4
	s_and_b64 s[34:35], s[18:19], s[34:35]
	s_or_b64 s[34:35], vcc, s[34:35]
	v_cndmask_b32_e64 v4, 0, 1, s[34:35]
	s_waitcnt lgkmcnt(3)
	v_cmp_eq_f32_e64 s[34:35], v3, v5
	v_cmp_lt_f32_e32 vcc, v3, v5
	s_and_b64 s[34:35], s[20:21], s[34:35]
	s_or_b64 s[34:35], vcc, s[34:35]
	v_cndmask_b32_e64 v5, 0, 1, s[34:35]
	s_waitcnt lgkmcnt(2)
	v_cmp_eq_f32_e64 s[34:35], v3, v6
	v_cmp_lt_f32_e32 vcc, v3, v6
	s_and_b64 s[34:35], s[22:23], s[34:35]
	s_or_b64 s[34:35], vcc, s[34:35]
	v_cndmask_b32_e64 v6, 0, 1, s[34:35]
	s_waitcnt lgkmcnt(1)
	v_cmp_eq_f32_e64 s[34:35], v3, v7
	v_cmp_lt_f32_e32 vcc, v3, v7
	s_and_b64 s[34:35], s[24:25], s[34:35]
	ds_bpermute_b32 v9, v100, v3
	s_or_b64 s[34:35], vcc, s[34:35]
	v_cndmask_b32_e64 v7, 0, 1, s[34:35]
	s_waitcnt lgkmcnt(1)
	v_cmp_eq_f32_e64 s[34:35], v3, v8
	v_cmp_lt_f32_e32 vcc, v3, v8
	s_and_b64 s[34:35], s[26:27], s[34:35]
	ds_bpermute_b32 v10, v101, v3
	s_or_b64 s[34:35], vcc, s[34:35]
	v_cndmask_b32_e64 v8, 0, 1, s[34:35]
	s_waitcnt lgkmcnt(1)
	v_cmp_eq_f32_e64 s[34:35], v3, v9
	ds_bpermute_b32 v11, v102, v3
	v_cmp_lt_f32_e32 vcc, v3, v9
	s_and_b64 s[34:35], s[28:29], s[34:35]
	s_or_b64 s[34:35], vcc, s[34:35]
	v_cndmask_b32_e64 v9, 0, 1, s[34:35]
	s_waitcnt lgkmcnt(1)
	v_cmp_eq_f32_e64 s[34:35], v3, v10
	v_cmp_lt_f32_e32 vcc, v3, v10
	s_and_b64 s[34:35], s[30:31], s[34:35]
	s_or_b64 s[34:35], vcc, s[34:35]
	s_waitcnt lgkmcnt(0)
	v_cmp_lt_f32_e32 vcc, v3, v11
	v_cndmask_b32_e64 v10, 0, 1, s[34:35]
	s_nop 0
	v_cndmask_b32_e64 v3, 0, 1, vcc
	v_add_u32_e32 v3, v5, v3
	v_add3_u32 v3, v3, v4, v6
	v_add3_u32 v3, v3, v7, v8
	v_add3_u32 v3, v3, v9, v10
	v_cmp_gt_u32_e32 vcc, 4, v3
	v_mov_b32_e32 v5, 0
	v_mov_b32_e32 v4, v104
	v_cndmask_b32_e32 v3, v110, v1, vcc

.LBB0_1889:
	s_or_b64 exec, exec, s[34:35]
	v_add_u32_e32 v1, s72, v84
	ds_read2st64_b32 v[2:3], v1 offset0:4 offset1:36
	s_mov_b32 s41, 0
	s_waitcnt lgkmcnt(0)
	v_add_f32_e32 v2, 0, v2
	v_add_f32_e32 v4, v2, v3
	ds_read2st64_b32 v[2:3], v1 offset0:68 offset1:100
	s_waitcnt lgkmcnt(0)
	v_add_f32_e32 v2, v4, v2
	v_add_f32_e32 v4, v2, v3
	ds_read2st64_b32 v[2:3], v1 offset0:132 offset1:164
	s_waitcnt lgkmcnt(0)
	v_add_f32_e32 v2, v4, v2
	v_add_f32_e32 v4, v2, v3
	ds_read2st64_b32 v[2:3], v1 offset0:196 offset1:228
	s_waitcnt lgkmcnt(0)
	v_add_f32_e32 v1, v4, v2
	v_add_f32_e32 v1, v1, v3
	v_mul_f32_e32 v2, 0xbfb8aa3b, v1
	v_fma_f32 v3, v1, s83, -v2
	v_rndne_f32_e32 v4, v2
	v_fmac_f32_e32 v3, 0xb2a5705f, v1
	v_sub_f32_e32 v2, v2, v4
	v_add_f32_e32 v2, v2, v3
	v_exp_f32_e32 v2, v2
	v_cvt_i32_f32_e32 v3, v4
	v_cmp_nlt_f32_e32 vcc, s84, v1
	v_ldexp_f32 v2, v2, v3
	s_nop 0
	v_cndmask_b32_e32 v2, 0, v2, vcc
	v_cmp_ngt_f32_e32 vcc, s85, v1
	s_nop 1
	v_cndmask_b32_e32 v1, v109, v2, vcc
	v_add_f32_e32 v1, 1.0, v1
	v_div_scale_f32 v2, s[34:35], v1, v1, 1.0
	v_rcp_f32_e32 v3, v2
	s_nop 0
	v_fma_f32 v4, -v2, v3, 1.0
	v_fmac_f32_e32 v3, v4, v3
	v_div_scale_f32 v4, vcc, 1.0, v1, 1.0
	v_mul_f32_e32 v5, v4, v3
	v_fma_f32 v6, -v2, v5, v4
	v_fmac_f32_e32 v5, v6, v3
	v_fma_f32 v2, -v2, v5, v4
	v_div_fmas_f32 v2, v2, v3, v5
	v_div_fixup_f32 v2, v2, v1, 1.0
	v_mov_b32_e32 v1, v128
	v_add_f32_e32 v3, v1, v2
	ds_bpermute_b32 v1, v88, v3
	ds_bpermute_b32 v4, v89, v3
	ds_bpermute_b32 v5, v90, v3
	ds_bpermute_b32 v6, v95, v3
	s_waitcnt lgkmcnt(3)
	v_cmp_eq_f32_e64 s[34:35], v3, v1
	v_cmp_lt_f32_e32 vcc, v3, v1
	s_and_b64 s[34:35], s[4:5], s[34:35]
	s_or_b64 s[34:35], vcc, s[34:35]
	v_cndmask_b32_e64 v1, 0, 1, s[34:35]
	s_waitcnt lgkmcnt(2)
	v_cmp_eq_f32_e64 s[34:35], v3, v4
	v_cmp_lt_f32_e32 vcc, v3, v4
	s_and_b64 s[34:35], s[6:7], s[34:35]
	s_or_b64 s[34:35], vcc, s[34:35]
	v_cndmask_b32_e64 v4, 0, 1, s[34:35]
	s_waitcnt lgkmcnt(1)
	v_cmp_eq_f32_e64 s[34:35], v3, v5
	v_cmp_lt_f32_e32 vcc, v3, v5
	s_and_b64 s[34:35], s[8:9], s[34:35]
	s_or_b64 s[34:35], vcc, s[34:35]
	v_cndmask_b32_e64 v5, 0, 1, s[34:35]
	v_add3_u32 v1, v1, v4, v5
	ds_bpermute_b32 v4, v91, v3
	ds_bpermute_b32 v5, v92, v3
	s_waitcnt lgkmcnt(1)
	v_cmp_eq_f32_e64 s[34:35], v3, v4
	v_cmp_lt_f32_e32 vcc, v3, v4
	s_and_b64 s[34:35], s[10:11], s[34:35]
	s_or_b64 s[34:35], vcc, s[34:35]
	v_cndmask_b32_e64 v4, 0, 1, s[34:35]
	s_waitcnt lgkmcnt(0)
	v_cmp_eq_f32_e64 s[34:35], v3, v5
	v_cmp_lt_f32_e32 vcc, v3, v5
	s_and_b64 s[34:35], s[12:13], s[34:35]
	s_or_b64 s[34:35], vcc, s[34:35]
	v_cndmask_b32_e64 v5, 0, 1, s[34:35]
	v_add3_u32 v1, v1, v4, v5
	ds_bpermute_b32 v4, v93, v3
	ds_bpermute_b32 v5, v94, v3
	s_waitcnt lgkmcnt(1)
	v_cmp_eq_f32_e64 s[34:35], v3, v4
	v_cmp_lt_f32_e32 vcc, v3, v4
	s_and_b64 s[34:35], s[14:15], s[34:35]
	s_or_b64 s[34:35], vcc, s[34:35]
	v_cndmask_b32_e64 v4, 0, 1, s[34:35]
	s_waitcnt lgkmcnt(0)
	v_cmp_eq_f32_e64 s[34:35], v3, v5
	v_cmp_lt_f32_e32 vcc, v3, v5
	s_and_b64 s[34:35], s[16:17], s[34:35]
	s_or_b64 s[34:35], vcc, s[34:35]
	v_cmp_lt_f32_e32 vcc, v3, v6
	v_cndmask_b32_e64 v5, 0, 1, s[34:35]
	s_nop 0
	v_addc_co_u32_e32 v1, vcc, v1, v4, vcc
	v_add_u32_e32 v1, v1, v5
	v_cmp_gt_u32_e32 vcc, 2, v1
	s_nop 1
	v_cndmask_b32_e32 v1, 0, v3, vcc
	ds_bpermute_b32 v4, v76, v1
	s_waitcnt lgkmcnt(0)
	v_add_f32_e32 v1, v1, v4
	ds_bpermute_b32 v4, v77, v1
	s_waitcnt lgkmcnt(0)
	v_add_f32_e32 v1, v1, v4
	ds_bpermute_b32 v4, v78, v1
	s_waitcnt lgkmcnt(0)
	v_add_f32_e32 v1, v1, v4
	ds_bpermute_b32 v4, v87, v1
	ds_bpermute_b32 v5, v96, v1
	ds_bpermute_b32 v6, v97, v1
	ds_bpermute_b32 v7, v98, v1
	ds_bpermute_b32 v8, v99, v1
	s_waitcnt lgkmcnt(4)
	v_cmp_eq_f32_e64 s[34:35], v1, v4
	v_cmp_lt_f32_e32 vcc, v1, v4
	s_and_b64 s[34:35], s[18:19], s[34:35]
	s_or_b64 s[34:35], vcc, s[34:35]
	v_cndmask_b32_e64 v4, 0, 1, s[34:35]
	s_waitcnt lgkmcnt(3)
	v_cmp_eq_f32_e64 s[34:35], v1, v5
	v_cmp_lt_f32_e32 vcc, v1, v5
	s_and_b64 s[34:35], s[20:21], s[34:35]
	s_or_b64 s[34:35], vcc, s[34:35]
	v_cndmask_b32_e64 v5, 0, 1, s[34:35]
	s_waitcnt lgkmcnt(2)
	v_cmp_eq_f32_e64 s[34:35], v1, v6
	v_cmp_lt_f32_e32 vcc, v1, v6
	s_and_b64 s[34:35], s[22:23], s[34:35]
	s_or_b64 s[34:35], vcc, s[34:35]
	v_cndmask_b32_e64 v6, 0, 1, s[34:35]
	s_waitcnt lgkmcnt(1)
	v_cmp_eq_f32_e64 s[34:35], v1, v7
	v_cmp_lt_f32_e32 vcc, v1, v7
	s_and_b64 s[34:35], s[24:25], s[34:35]
	ds_bpermute_b32 v9, v100, v1
	s_or_b64 s[34:35], vcc, s[34:35]
	v_cndmask_b32_e64 v7, 0, 1, s[34:35]
	s_waitcnt lgkmcnt(1)
	v_cmp_eq_f32_e64 s[34:35], v1, v8
	v_cmp_lt_f32_e32 vcc, v1, v8
	s_and_b64 s[34:35], s[26:27], s[34:35]
	ds_bpermute_b32 v10, v101, v1
	s_or_b64 s[34:35], vcc, s[34:35]
	v_cndmask_b32_e64 v8, 0, 1, s[34:35]
	s_waitcnt lgkmcnt(1)
	v_cmp_eq_f32_e64 s[34:35], v1, v9
	ds_bpermute_b32 v11, v102, v1
	v_cmp_lt_f32_e32 vcc, v1, v9
	s_and_b64 s[34:35], s[28:29], s[34:35]
	s_or_b64 s[34:35], vcc, s[34:35]
	v_cndmask_b32_e64 v9, 0, 1, s[34:35]
	s_waitcnt lgkmcnt(1)
	v_cmp_eq_f32_e64 s[34:35], v1, v10
	v_cmp_lt_f32_e32 vcc, v1, v10
	s_and_b64 s[34:35], s[30:31], s[34:35]
	s_or_b64 s[34:35], vcc, s[34:35]
	s_waitcnt lgkmcnt(0)
	v_cmp_lt_f32_e32 vcc, v1, v11
	v_cndmask_b32_e64 v10, 0, 1, s[34:35]
	s_nop 0
	v_cndmask_b32_e64 v1, 0, 1, vcc
	v_add_u32_e32 v1, v5, v1
	v_add3_u32 v1, v1, v4, v6
	v_add3_u32 v1, v1, v7, v8
	v_add3_u32 v1, v1, v9, v10
	v_cmp_gt_u32_e32 vcc, 4, v1
	v_mov_b32_e32 v5, 0
	v_mov_b32_e32 v4, v104
	v_cndmask_b32_e32 v3, v110, v3, vcc

.LBB0_1893:
	s_or_b64 exec, exec, s[34:35]
	v_add_u32_e32 v1, s75, v84
	ds_read2st64_b32 v[2:3], v1 offset0:4 offset1:36
	s_mov_b32 s41, 0
	s_waitcnt lgkmcnt(0)
	v_add_f32_e32 v2, 0, v2
	v_add_f32_e32 v4, v2, v3
	ds_read2st64_b32 v[2:3], v1 offset0:68 offset1:100
	s_waitcnt lgkmcnt(0)
	v_add_f32_e32 v2, v4, v2
	v_add_f32_e32 v4, v2, v3
	ds_read2st64_b32 v[2:3], v1 offset0:132 offset1:164
	s_waitcnt lgkmcnt(0)
	v_add_f32_e32 v2, v4, v2
	v_add_f32_e32 v4, v2, v3
	ds_read2st64_b32 v[2:3], v1 offset0:196 offset1:228
	s_waitcnt lgkmcnt(0)
	v_add_f32_e32 v1, v4, v2
	v_add_f32_e32 v1, v1, v3
	v_mul_f32_e32 v2, 0xbfb8aa3b, v1
	v_fma_f32 v3, v1, s83, -v2
	v_rndne_f32_e32 v4, v2
	v_fmac_f32_e32 v3, 0xb2a5705f, v1
	v_sub_f32_e32 v2, v2, v4
	v_add_f32_e32 v2, v2, v3
	v_exp_f32_e32 v2, v2
	v_cvt_i32_f32_e32 v3, v4
	v_cmp_nlt_f32_e32 vcc, s84, v1
	v_ldexp_f32 v2, v2, v3
	s_nop 0
	v_cndmask_b32_e32 v2, 0, v2, vcc
	v_cmp_ngt_f32_e32 vcc, s85, v1
	s_nop 1
	v_cndmask_b32_e32 v1, v109, v2, vcc
	v_add_f32_e32 v1, 1.0, v1
	v_div_scale_f32 v2, s[34:35], v1, v1, 1.0
	v_rcp_f32_e32 v3, v2
	s_nop 0
	v_fma_f32 v4, -v2, v3, 1.0
	v_fmac_f32_e32 v3, v4, v3
	v_div_scale_f32 v4, vcc, 1.0, v1, 1.0
	v_mul_f32_e32 v5, v4, v3
	v_fma_f32 v6, -v2, v5, v4
	v_fmac_f32_e32 v5, v6, v3
	v_fma_f32 v2, -v2, v5, v4
	v_div_fmas_f32 v2, v2, v3, v5
	v_div_fixup_f32 v2, v2, v1, 1.0
	v_mov_b32_e32 v1, v128
	v_add_f32_e32 v3, v1, v2
	ds_bpermute_b32 v1, v88, v3
	ds_bpermute_b32 v4, v89, v3
	ds_bpermute_b32 v5, v90, v3
	ds_bpermute_b32 v6, v95, v3
	s_waitcnt lgkmcnt(3)
	v_cmp_eq_f32_e64 s[34:35], v3, v1
	v_cmp_lt_f32_e32 vcc, v3, v1
	s_and_b64 s[34:35], s[4:5], s[34:35]
	s_or_b64 s[34:35], vcc, s[34:35]
	v_cndmask_b32_e64 v1, 0, 1, s[34:35]
	s_waitcnt lgkmcnt(2)
	v_cmp_eq_f32_e64 s[34:35], v3, v4
	v_cmp_lt_f32_e32 vcc, v3, v4
	s_and_b64 s[34:35], s[6:7], s[34:35]
	s_or_b64 s[34:35], vcc, s[34:35]
	v_cndmask_b32_e64 v4, 0, 1, s[34:35]
	s_waitcnt lgkmcnt(1)
	v_cmp_eq_f32_e64 s[34:35], v3, v5
	v_cmp_lt_f32_e32 vcc, v3, v5
	s_and_b64 s[34:35], s[8:9], s[34:35]
	s_or_b64 s[34:35], vcc, s[34:35]
	v_cndmask_b32_e64 v5, 0, 1, s[34:35]
	v_add3_u32 v1, v1, v4, v5
	ds_bpermute_b32 v4, v91, v3
	ds_bpermute_b32 v5, v92, v3
	s_waitcnt lgkmcnt(1)
	v_cmp_eq_f32_e64 s[34:35], v3, v4
	v_cmp_lt_f32_e32 vcc, v3, v4
	s_and_b64 s[34:35], s[10:11], s[34:35]
	s_or_b64 s[34:35], vcc, s[34:35]
	v_cndmask_b32_e64 v4, 0, 1, s[34:35]
	s_waitcnt lgkmcnt(0)
	v_cmp_eq_f32_e64 s[34:35], v3, v5
	v_cmp_lt_f32_e32 vcc, v3, v5
	s_and_b64 s[34:35], s[12:13], s[34:35]
	s_or_b64 s[34:35], vcc, s[34:35]
	v_cndmask_b32_e64 v5, 0, 1, s[34:35]
	v_add3_u32 v1, v1, v4, v5
	ds_bpermute_b32 v4, v93, v3
	ds_bpermute_b32 v5, v94, v3
	s_waitcnt lgkmcnt(1)
	v_cmp_eq_f32_e64 s[34:35], v3, v4
	v_cmp_lt_f32_e32 vcc, v3, v4
	s_and_b64 s[34:35], s[14:15], s[34:35]
	s_or_b64 s[34:35], vcc, s[34:35]
	v_cndmask_b32_e64 v4, 0, 1, s[34:35]
	s_waitcnt lgkmcnt(0)
	v_cmp_eq_f32_e64 s[34:35], v3, v5
	v_cmp_lt_f32_e32 vcc, v3, v5
	s_and_b64 s[34:35], s[16:17], s[34:35]
	s_or_b64 s[34:35], vcc, s[34:35]
	v_cmp_lt_f32_e32 vcc, v3, v6
	v_cndmask_b32_e64 v5, 0, 1, s[34:35]
	s_nop 0
	v_addc_co_u32_e32 v1, vcc, v1, v4, vcc
	v_add_u32_e32 v1, v1, v5
	v_cmp_gt_u32_e32 vcc, 2, v1
	s_nop 1
	v_cndmask_b32_e32 v1, 0, v3, vcc
	ds_bpermute_b32 v4, v76, v1
	s_waitcnt lgkmcnt(0)
	v_add_f32_e32 v1, v1, v4
	ds_bpermute_b32 v4, v77, v1
	s_waitcnt lgkmcnt(0)
	v_add_f32_e32 v1, v1, v4
	ds_bpermute_b32 v4, v78, v1
	s_waitcnt lgkmcnt(0)
	v_add_f32_e32 v1, v1, v4
	ds_bpermute_b32 v4, v87, v1
	ds_bpermute_b32 v5, v96, v1
	ds_bpermute_b32 v6, v97, v1
	ds_bpermute_b32 v7, v98, v1
	ds_bpermute_b32 v8, v99, v1
	s_waitcnt lgkmcnt(4)
	v_cmp_eq_f32_e64 s[34:35], v1, v4
	v_cmp_lt_f32_e32 vcc, v1, v4
	s_and_b64 s[34:35], s[18:19], s[34:35]
	s_or_b64 s[34:35], vcc, s[34:35]
	v_cndmask_b32_e64 v4, 0, 1, s[34:35]
	s_waitcnt lgkmcnt(3)
	v_cmp_eq_f32_e64 s[34:35], v1, v5
	v_cmp_lt_f32_e32 vcc, v1, v5
	s_and_b64 s[34:35], s[20:21], s[34:35]
	s_or_b64 s[34:35], vcc, s[34:35]
	v_cndmask_b32_e64 v5, 0, 1, s[34:35]
	s_waitcnt lgkmcnt(2)
	v_cmp_eq_f32_e64 s[34:35], v1, v6
	v_cmp_lt_f32_e32 vcc, v1, v6
	s_and_b64 s[34:35], s[22:23], s[34:35]
	s_or_b64 s[34:35], vcc, s[34:35]
	v_cndmask_b32_e64 v6, 0, 1, s[34:35]
	s_waitcnt lgkmcnt(1)
	v_cmp_eq_f32_e64 s[34:35], v1, v7
	v_cmp_lt_f32_e32 vcc, v1, v7
	s_and_b64 s[34:35], s[24:25], s[34:35]
	ds_bpermute_b32 v9, v100, v1
	s_or_b64 s[34:35], vcc, s[34:35]
	v_cndmask_b32_e64 v7, 0, 1, s[34:35]
	s_waitcnt lgkmcnt(1)
	v_cmp_eq_f32_e64 s[34:35], v1, v8
	v_cmp_lt_f32_e32 vcc, v1, v8
	s_and_b64 s[34:35], s[26:27], s[34:35]
	ds_bpermute_b32 v10, v101, v1
	s_or_b64 s[34:35], vcc, s[34:35]
	v_cndmask_b32_e64 v8, 0, 1, s[34:35]
	s_waitcnt lgkmcnt(1)
	v_cmp_eq_f32_e64 s[34:35], v1, v9
	ds_bpermute_b32 v11, v102, v1
	v_cmp_lt_f32_e32 vcc, v1, v9
	s_and_b64 s[34:35], s[28:29], s[34:35]
	s_or_b64 s[34:35], vcc, s[34:35]
	v_cndmask_b32_e64 v9, 0, 1, s[34:35]
	s_waitcnt lgkmcnt(1)
	v_cmp_eq_f32_e64 s[34:35], v1, v10
	v_cmp_lt_f32_e32 vcc, v1, v10
	s_and_b64 s[34:35], s[30:31], s[34:35]
	s_or_b64 s[34:35], vcc, s[34:35]
	s_waitcnt lgkmcnt(0)
	v_cmp_lt_f32_e32 vcc, v1, v11
	v_cndmask_b32_e64 v10, 0, 1, s[34:35]
	s_nop 0
	v_cndmask_b32_e64 v1, 0, 1, vcc
	v_add_u32_e32 v1, v5, v1
	v_add3_u32 v1, v1, v4, v6
	v_add3_u32 v1, v1, v7, v8
	v_add3_u32 v1, v1, v9, v10
	v_cmp_gt_u32_e32 vcc, 4, v1
	v_mov_b32_e32 v5, 0
	v_mov_b32_e32 v4, v104
	v_cndmask_b32_e32 v3, v110, v3, vcc

.LBB0_1897:
	s_or_b64 exec, exec, s[34:35]
	v_add_u32_e32 v1, s79, v84
	ds_read2st64_b32 v[2:3], v1 offset0:4 offset1:36
	s_mov_b32 s41, 0
	s_waitcnt lgkmcnt(0)
	v_add_f32_e32 v2, 0, v2
	v_add_f32_e32 v4, v2, v3
	ds_read2st64_b32 v[2:3], v1 offset0:68 offset1:100
	s_waitcnt lgkmcnt(0)
	v_add_f32_e32 v2, v4, v2
	v_add_f32_e32 v4, v2, v3
	ds_read2st64_b32 v[2:3], v1 offset0:132 offset1:164
	s_waitcnt lgkmcnt(0)
	v_add_f32_e32 v2, v4, v2
	v_add_f32_e32 v4, v2, v3
	ds_read2st64_b32 v[2:3], v1 offset0:196 offset1:228
	s_waitcnt lgkmcnt(0)
	v_add_f32_e32 v1, v4, v2
	v_add_f32_e32 v1, v1, v3
	v_mul_f32_e32 v2, 0xbfb8aa3b, v1
	v_fma_f32 v3, v1, s83, -v2
	v_rndne_f32_e32 v4, v2
	v_fmac_f32_e32 v3, 0xb2a5705f, v1
	v_sub_f32_e32 v2, v2, v4
	v_add_f32_e32 v2, v2, v3
	v_exp_f32_e32 v2, v2
	v_cvt_i32_f32_e32 v3, v4
	v_cmp_nlt_f32_e32 vcc, s84, v1
	v_ldexp_f32 v2, v2, v3
	s_nop 0
	v_cndmask_b32_e32 v2, 0, v2, vcc
	v_cmp_ngt_f32_e32 vcc, s85, v1
	s_nop 1
	v_cndmask_b32_e32 v1, v109, v2, vcc
	v_add_f32_e32 v1, 1.0, v1
	v_div_scale_f32 v2, s[34:35], v1, v1, 1.0
	v_rcp_f32_e32 v3, v2
	s_nop 0
	v_fma_f32 v4, -v2, v3, 1.0
	v_fmac_f32_e32 v3, v4, v3
	v_div_scale_f32 v4, vcc, 1.0, v1, 1.0
	v_mul_f32_e32 v5, v4, v3
	v_fma_f32 v6, -v2, v5, v4
	v_fmac_f32_e32 v5, v6, v3
	v_fma_f32 v2, -v2, v5, v4
	v_div_fmas_f32 v2, v2, v3, v5
	v_div_fixup_f32 v2, v2, v1, 1.0
	v_mov_b32_e32 v1, v128
	v_add_f32_e32 v3, v1, v2
	ds_bpermute_b32 v1, v88, v3
	ds_bpermute_b32 v4, v89, v3
	ds_bpermute_b32 v5, v90, v3
	ds_bpermute_b32 v6, v95, v3
	s_waitcnt lgkmcnt(3)
	v_cmp_eq_f32_e64 s[34:35], v3, v1
	v_cmp_lt_f32_e32 vcc, v3, v1
	s_and_b64 s[34:35], s[4:5], s[34:35]
	s_or_b64 s[34:35], vcc, s[34:35]
	v_cndmask_b32_e64 v1, 0, 1, s[34:35]
	s_waitcnt lgkmcnt(2)
	v_cmp_eq_f32_e64 s[34:35], v3, v4
	v_cmp_lt_f32_e32 vcc, v3, v4
	s_and_b64 s[34:35], s[6:7], s[34:35]
	s_or_b64 s[34:35], vcc, s[34:35]
	v_cndmask_b32_e64 v4, 0, 1, s[34:35]
	s_waitcnt lgkmcnt(1)
	v_cmp_eq_f32_e64 s[34:35], v3, v5
	v_cmp_lt_f32_e32 vcc, v3, v5
	s_and_b64 s[34:35], s[8:9], s[34:35]
	s_or_b64 s[34:35], vcc, s[34:35]
	v_cndmask_b32_e64 v5, 0, 1, s[34:35]
	v_add3_u32 v1, v1, v4, v5
	ds_bpermute_b32 v4, v91, v3
	ds_bpermute_b32 v5, v92, v3
	s_waitcnt lgkmcnt(1)
	v_cmp_eq_f32_e64 s[34:35], v3, v4
	v_cmp_lt_f32_e32 vcc, v3, v4
	s_and_b64 s[34:35], s[10:11], s[34:35]
	s_or_b64 s[34:35], vcc, s[34:35]
	v_cndmask_b32_e64 v4, 0, 1, s[34:35]
	s_waitcnt lgkmcnt(0)
	v_cmp_eq_f32_e64 s[34:35], v3, v5
	v_cmp_lt_f32_e32 vcc, v3, v5
	s_and_b64 s[34:35], s[12:13], s[34:35]
	s_or_b64 s[34:35], vcc, s[34:35]
	v_cndmask_b32_e64 v5, 0, 1, s[34:35]
	v_add3_u32 v1, v1, v4, v5
	ds_bpermute_b32 v4, v93, v3
	ds_bpermute_b32 v5, v94, v3
	s_waitcnt lgkmcnt(1)
	v_cmp_eq_f32_e64 s[34:35], v3, v4
	v_cmp_lt_f32_e32 vcc, v3, v4
	s_and_b64 s[34:35], s[14:15], s[34:35]
	s_or_b64 s[34:35], vcc, s[34:35]
	v_cndmask_b32_e64 v4, 0, 1, s[34:35]
	s_waitcnt lgkmcnt(0)
	v_cmp_eq_f32_e64 s[34:35], v3, v5
	v_cmp_lt_f32_e32 vcc, v3, v5
	s_and_b64 s[34:35], s[16:17], s[34:35]
	s_or_b64 s[34:35], vcc, s[34:35]
	v_cmp_lt_f32_e32 vcc, v3, v6
	v_cndmask_b32_e64 v5, 0, 1, s[34:35]
	s_nop 0
	v_addc_co_u32_e32 v1, vcc, v1, v4, vcc
	v_add_u32_e32 v1, v1, v5
	v_cmp_gt_u32_e32 vcc, 2, v1
	s_nop 1
	v_cndmask_b32_e32 v1, 0, v3, vcc
	ds_bpermute_b32 v4, v76, v1
	s_waitcnt lgkmcnt(0)
	v_add_f32_e32 v1, v1, v4
	ds_bpermute_b32 v4, v77, v1
	s_waitcnt lgkmcnt(0)
	v_add_f32_e32 v1, v1, v4
	ds_bpermute_b32 v4, v78, v1
	s_waitcnt lgkmcnt(0)
	v_add_f32_e32 v1, v1, v4
	ds_bpermute_b32 v4, v87, v1
	ds_bpermute_b32 v5, v96, v1
	ds_bpermute_b32 v6, v97, v1
	ds_bpermute_b32 v7, v98, v1
	ds_bpermute_b32 v8, v99, v1
	s_waitcnt lgkmcnt(4)
	v_cmp_eq_f32_e64 s[34:35], v1, v4
	v_cmp_lt_f32_e32 vcc, v1, v4
	s_and_b64 s[34:35], s[18:19], s[34:35]
	s_or_b64 s[34:35], vcc, s[34:35]
	v_cndmask_b32_e64 v4, 0, 1, s[34:35]
	s_waitcnt lgkmcnt(3)
	v_cmp_eq_f32_e64 s[34:35], v1, v5
	v_cmp_lt_f32_e32 vcc, v1, v5
	s_and_b64 s[34:35], s[20:21], s[34:35]
	s_or_b64 s[34:35], vcc, s[34:35]
	v_cndmask_b32_e64 v5, 0, 1, s[34:35]
	s_waitcnt lgkmcnt(2)
	v_cmp_eq_f32_e64 s[34:35], v1, v6
	v_cmp_lt_f32_e32 vcc, v1, v6
	s_and_b64 s[34:35], s[22:23], s[34:35]
	s_or_b64 s[34:35], vcc, s[34:35]
	v_cndmask_b32_e64 v6, 0, 1, s[34:35]
	s_waitcnt lgkmcnt(1)
	v_cmp_eq_f32_e64 s[34:35], v1, v7
	v_cmp_lt_f32_e32 vcc, v1, v7
	s_and_b64 s[34:35], s[24:25], s[34:35]
	ds_bpermute_b32 v9, v100, v1
	s_or_b64 s[34:35], vcc, s[34:35]
	v_cndmask_b32_e64 v7, 0, 1, s[34:35]
	s_waitcnt lgkmcnt(1)
	v_cmp_eq_f32_e64 s[34:35], v1, v8
	v_cmp_lt_f32_e32 vcc, v1, v8
	s_and_b64 s[34:35], s[26:27], s[34:35]
	ds_bpermute_b32 v10, v101, v1
	s_or_b64 s[34:35], vcc, s[34:35]
	v_cndmask_b32_e64 v8, 0, 1, s[34:35]
	s_waitcnt lgkmcnt(1)
	v_cmp_eq_f32_e64 s[34:35], v1, v9
	ds_bpermute_b32 v11, v102, v1
	v_cmp_lt_f32_e32 vcc, v1, v9
	s_and_b64 s[34:35], s[28:29], s[34:35]
	s_or_b64 s[34:35], vcc, s[34:35]
	v_cndmask_b32_e64 v9, 0, 1, s[34:35]
	s_waitcnt lgkmcnt(1)
	v_cmp_eq_f32_e64 s[34:35], v1, v10
	v_cmp_lt_f32_e32 vcc, v1, v10
	s_and_b64 s[34:35], s[30:31], s[34:35]
	s_or_b64 s[34:35], vcc, s[34:35]
	s_waitcnt lgkmcnt(0)
	v_cmp_lt_f32_e32 vcc, v1, v11
	v_cndmask_b32_e64 v10, 0, 1, s[34:35]
	s_nop 0
	v_cndmask_b32_e64 v1, 0, 1, vcc
	v_add_u32_e32 v1, v5, v1
	v_add3_u32 v1, v1, v4, v6
	v_add3_u32 v1, v1, v7, v8
	v_add3_u32 v1, v1, v9, v10
	v_cmp_gt_u32_e32 vcc, 4, v1
	v_mov_b32_e32 v5, 0
	v_mov_b32_e32 v4, v104
	v_cndmask_b32_e32 v3, v110, v3, vcc
